# fp8 GEMM K-loops: unit-scale v_mfma_scale replaced by the unscaled v_mfma_f32_16x16x128_f8f6f4 (same fp8 e4m3 operands, f32 accumulate), on top of v062
# speedup vs baseline: 1.0027x; 1.0027x over previous
.LBB0_202:
	ds_read_b128 v[2:5], v172
	ds_read_b128 v[6:9], v172 offset:1024
	ds_read_b128 v[10:13], v172 offset:2048
	ds_read_b128 v[14:17], v172 offset:3072
	s_add_u32 s34, s30, 0xfffc0080
	s_addc_u32 s35, s31, -1
	s_cmp_eq_u32 s56, 12
	s_cselect_b32 s37, s21, s35
	s_cselect_b32 s36, s52, s34
	s_cselect_b32 s35, s11, s55
	s_cselect_b32 s34, s53, s54
	s_add_i32 m0, s29, 0xc000
	ds_read_b128 v[176:179], v173
	ds_read_b128 v[180:183], v173 offset:1024
	ds_read_b128 v[184:187], v173 offset:2048
	ds_read_b128 v[188:191], v173 offset:3072
	ds_read_b128 v[192:195], v173 offset:4096
	ds_read_b128 v[196:199], v173 offset:5120
	ds_read_b128 v[206:209], v173 offset:6144
	ds_read_b128 v[210:213], v173 offset:7168
	global_load_lds_dwordx4 v154, s[30:31]
	s_add_i32 m0, s29, 0xe000
	s_nop 0
	global_load_lds_dwordx4 v156, s[30:31]
	s_waitcnt lgkmcnt(8)
	s_barrier
	s_waitcnt lgkmcnt(0)
	s_setprio 1
	s_waitcnt lgkmcnt(0)
	v_mfma_f32_16x16x128_f8f6f4 v[142:145], v[2:9], v[176:183], v[142:145]
	v_mfma_f32_16x16x128_f8f6f4 v[138:141], v[10:17], v[176:183], v[138:141]
	v_mfma_f32_16x16x128_f8f6f4 v[134:137], v[2:9], v[184:191], v[134:137]
	v_mfma_f32_16x16x128_f8f6f4 v[126:129], v[10:17], v[184:191], v[126:129]
	v_mfma_f32_16x16x128_f8f6f4 v[118:121], v[2:9], v[192:199], v[118:121]
	v_mfma_f32_16x16x128_f8f6f4 v[110:113], v[10:17], v[192:199], v[110:113]
	v_mfma_f32_16x16x128_f8f6f4 v[102:105], v[2:9], v[206:213], v[102:105]
	v_mfma_f32_16x16x128_f8f6f4 v[94:97], v[10:17], v[206:213], v[94:97]
	s_setprio 0
	s_barrier
	s_add_i32 s57, s48, s38
	s_add_u32 s66, s34, 0x80
	s_addc_u32 s67, s35, 0
	s_mov_b32 m0, s57
	ds_read_b128 v[214:217], v175
	ds_read_b128 v[218:221], v175 offset:1024
	ds_read_b128 v[222:225], v175 offset:2048
	ds_read_b128 v[226:229], v175 offset:3072
	global_load_lds_dwordx4 v150, s[34:35]
	s_add_i32 m0, s57, 0x2000
	s_nop 0
	global_load_lds_dwordx4 v146, s[34:35]
	s_barrier
	s_waitcnt lgkmcnt(0)
	s_setprio 1
	s_waitcnt lgkmcnt(0)
	v_mfma_f32_16x16x128_f8f6f4 v[130:133], v[214:221], v[176:183], v[130:133]
	v_mfma_f32_16x16x128_f8f6f4 v[122:125], v[222:229], v[176:183], v[122:125]
	v_mfma_f32_16x16x128_f8f6f4 v[114:117], v[214:221], v[184:191], v[114:117]
	v_mfma_f32_16x16x128_f8f6f4 v[106:109], v[222:229], v[184:191], v[106:109]
	v_mfma_f32_16x16x128_f8f6f4 v[98:101], v[214:221], v[192:199], v[98:101]
	v_mfma_f32_16x16x128_f8f6f4 v[90:93], v[222:229], v[192:199], v[90:93]
	v_mfma_f32_16x16x128_f8f6f4 v[86:89], v[214:221], v[206:213], v[86:89]
	v_mfma_f32_16x16x128_f8f6f4 v[82:85], v[222:229], v[206:213], v[82:85]
	s_setprio 0
	s_mov_b32 m0, s29
	s_add_u32 s68, s36, 0x80
	s_addc_u32 s69, s37, 0
	s_barrier
	ds_read_b128 v[176:179], v173 offset:16384
	ds_read_b128 v[180:183], v173 offset:17408
	ds_read_b128 v[184:187], v173 offset:18432
	ds_read_b128 v[188:191], v173 offset:19456
	ds_read_b128 v[192:195], v173 offset:20480
	ds_read_b128 v[196:199], v173 offset:21504
	ds_read_b128 v[206:209], v173 offset:22528
	ds_read_b128 v[210:213], v173 offset:23552
	global_load_lds_dwordx4 v152, s[36:37]
	s_mov_b32 m0, s41
	s_nop 0
	global_load_lds_dwordx4 v148, s[36:37]
	s_barrier
	s_waitcnt lgkmcnt(0)
	s_setprio 1
	s_waitcnt lgkmcnt(0)
	v_mfma_f32_16x16x128_f8f6f4 v[78:81], v[2:9], v[176:183], v[78:81]
	v_mfma_f32_16x16x128_f8f6f4 v[74:77], v[10:17], v[176:183], v[74:77]
	v_mfma_f32_16x16x128_f8f6f4 v[70:73], v[2:9], v[184:191], v[70:73]
	v_mfma_f32_16x16x128_f8f6f4 v[62:65], v[10:17], v[184:191], v[62:65]
	v_mfma_f32_16x16x128_f8f6f4 v[54:57], v[2:9], v[192:199], v[54:57]
	v_mfma_f32_16x16x128_f8f6f4 v[46:49], v[10:17], v[192:199], v[46:49]
	v_mfma_f32_16x16x128_f8f6f4 v[38:41], v[2:9], v[206:213], v[38:41]
	v_mfma_f32_16x16x128_f8f6f4 v[30:33], v[10:17], v[206:213], v[30:33]
	s_setprio 0
	s_barrier
	s_add_u32 s60, s34, 0x40000
	s_addc_u32 s61, s35, 0
	s_add_i32 s57, s49, s38
	s_mov_b32 m0, s57
	s_nop 0
	global_load_lds_dwordx4 v150, s[60:61]
	s_add_i32 m0, s57, 0x2000
	s_nop 0
	global_load_lds_dwordx4 v146, s[60:61]
	s_waitcnt vmcnt(6)
	s_barrier
	s_setprio 1
	v_mfma_f32_16x16x128_f8f6f4 v[66:69], v[214:221], v[176:183], v[66:69]
	v_mfma_f32_16x16x128_f8f6f4 v[58:61], v[222:229], v[176:183], v[58:61]
	v_mfma_f32_16x16x128_f8f6f4 v[50:53], v[214:221], v[184:191], v[50:53]
	v_mfma_f32_16x16x128_f8f6f4 v[42:45], v[222:229], v[184:191], v[42:45]
	v_mfma_f32_16x16x128_f8f6f4 v[34:37], v[214:221], v[192:199], v[34:37]
	v_mfma_f32_16x16x128_f8f6f4 v[26:29], v[222:229], v[192:199], v[26:29]
	v_mfma_f32_16x16x128_f8f6f4 v[22:25], v[214:221], v[206:213], v[22:25]
	v_mfma_f32_16x16x128_f8f6f4 v[18:21], v[222:229], v[206:213], v[18:21]
	s_setprio 0
	s_add_i32 s57, 0, 0x18000
	v_add_u32_e32 v14, s57, v170
	s_barrier
	ds_read_b128 v[2:5], v14
	ds_read_b128 v[6:9], v14 offset:1024
	ds_read_b128 v[10:13], v14 offset:2048
	ds_read_b128 v[14:17], v14 offset:3072
	s_add_u32 s36, s36, 0x40000
	s_addc_u32 s37, s37, 0
	s_mov_b32 m0, s42
	ds_read_b128 v[176:179], v173 offset:32768
	ds_read_b128 v[180:183], v173 offset:33792
	ds_read_b128 v[184:187], v173 offset:34816
	ds_read_b128 v[188:191], v173 offset:35840
	ds_read_b128 v[192:195], v173 offset:36864
	ds_read_b128 v[196:199], v173 offset:37888
	ds_read_b128 v[206:209], v173 offset:38912
	ds_read_b128 v[210:213], v173 offset:39936
	global_load_lds_dwordx4 v152, s[36:37]
	s_mov_b32 m0, s43
	s_nop 0
	global_load_lds_dwordx4 v148, s[36:37]
	s_waitcnt lgkmcnt(8)
	s_barrier
	s_waitcnt lgkmcnt(0)
	s_setprio 1
	s_waitcnt lgkmcnt(0)
	v_mfma_f32_16x16x128_f8f6f4 v[142:145], v[2:9], v[176:183], v[142:145]
	v_mfma_f32_16x16x128_f8f6f4 v[138:141], v[10:17], v[176:183], v[138:141]
	v_mfma_f32_16x16x128_f8f6f4 v[134:137], v[2:9], v[184:191], v[134:137]
	v_mfma_f32_16x16x128_f8f6f4 v[126:129], v[10:17], v[184:191], v[126:129]
	v_mfma_f32_16x16x128_f8f6f4 v[118:121], v[2:9], v[192:199], v[118:121]
	v_mfma_f32_16x16x128_f8f6f4 v[110:113], v[10:17], v[192:199], v[110:113]
	v_mfma_f32_16x16x128_f8f6f4 v[102:105], v[2:9], v[206:213], v[102:105]
	v_mfma_f32_16x16x128_f8f6f4 v[94:97], v[10:17], v[206:213], v[94:97]
	s_setprio 0
	s_barrier
	s_add_i32 s36, 0, 0x1c000
	s_add_i32 s37, s57, s38
	v_add_u32_e32 v200, s36, v170
	s_mov_b32 m0, s37
	ds_read_b128 v[214:217], v200
	ds_read_b128 v[218:221], v200 offset:1024
	ds_read_b128 v[222:225], v200 offset:2048
	ds_read_b128 v[226:229], v200 offset:3072
	global_load_lds_dwordx4 v150, s[66:67]
	s_add_i32 m0, s37, 0x2000
	s_nop 0
	global_load_lds_dwordx4 v146, s[66:67]
	s_barrier
	s_waitcnt lgkmcnt(0)
	s_setprio 1
	s_waitcnt lgkmcnt(0)
	v_mfma_f32_16x16x128_f8f6f4 v[130:133], v[214:221], v[176:183], v[130:133]
	v_mfma_f32_16x16x128_f8f6f4 v[122:125], v[222:229], v[176:183], v[122:125]
	v_mfma_f32_16x16x128_f8f6f4 v[114:117], v[214:221], v[184:191], v[114:117]
	v_mfma_f32_16x16x128_f8f6f4 v[106:109], v[222:229], v[184:191], v[106:109]
	v_mfma_f32_16x16x128_f8f6f4 v[98:101], v[214:221], v[192:199], v[98:101]
	v_mfma_f32_16x16x128_f8f6f4 v[90:93], v[222:229], v[192:199], v[90:93]
	v_mfma_f32_16x16x128_f8f6f4 v[86:89], v[214:221], v[206:213], v[86:89]
	v_mfma_f32_16x16x128_f8f6f4 v[82:85], v[222:229], v[206:213], v[82:85]
	s_setprio 0
	s_mov_b32 m0, s45
	s_barrier
	ds_read_b128 v[176:179], v173 offset:49152
	ds_read_b128 v[180:183], v173 offset:50176
	ds_read_b128 v[184:187], v173 offset:51200
	ds_read_b128 v[188:191], v173 offset:52224
	ds_read_b128 v[192:195], v173 offset:53248
	ds_read_b128 v[196:199], v173 offset:54272
	ds_read_b128 v[206:209], v173 offset:55296
	ds_read_b128 v[210:213], v173 offset:56320
	global_load_lds_dwordx4 v152, s[68:69]
	s_mov_b32 m0, s46
	s_nop 0
	global_load_lds_dwordx4 v148, s[68:69]
	s_barrier
	s_waitcnt lgkmcnt(0)
	s_setprio 1
	s_waitcnt lgkmcnt(0)
	v_mfma_f32_16x16x128_f8f6f4 v[78:81], v[2:9], v[176:183], v[78:81]
	v_mfma_f32_16x16x128_f8f6f4 v[74:77], v[10:17], v[176:183], v[74:77]
	v_mfma_f32_16x16x128_f8f6f4 v[70:73], v[2:9], v[184:191], v[70:73]
	v_mfma_f32_16x16x128_f8f6f4 v[62:65], v[10:17], v[184:191], v[62:65]
	v_mfma_f32_16x16x128_f8f6f4 v[54:57], v[2:9], v[192:199], v[54:57]
	v_mfma_f32_16x16x128_f8f6f4 v[46:49], v[10:17], v[192:199], v[46:49]
	v_mfma_f32_16x16x128_f8f6f4 v[38:41], v[2:9], v[206:213], v[38:41]
	v_mfma_f32_16x16x128_f8f6f4 v[30:33], v[10:17], v[206:213], v[30:33]
	s_setprio 0
	s_barrier
	s_add_u32 s34, s34, 0x40080
	s_addc_u32 s35, s35, 0
	s_add_i32 s36, s36, s38
	s_mov_b32 m0, s36
	s_nop 0
	global_load_lds_dwordx4 v150, s[34:35]
	s_add_i32 m0, s36, 0x2000
	s_nop 0
	global_load_lds_dwordx4 v146, s[34:35]
	s_waitcnt vmcnt(6)
	s_barrier
	s_setprio 1
	v_mfma_f32_16x16x128_f8f6f4 v[66:69], v[214:221], v[176:183], v[66:69]
	v_mfma_f32_16x16x128_f8f6f4 v[58:61], v[222:229], v[176:183], v[58:61]
	v_mfma_f32_16x16x128_f8f6f4 v[50:53], v[214:221], v[184:191], v[50:53]
	v_mfma_f32_16x16x128_f8f6f4 v[42:45], v[222:229], v[184:191], v[42:45]
	v_mfma_f32_16x16x128_f8f6f4 v[34:37], v[214:221], v[192:199], v[34:37]
	v_mfma_f32_16x16x128_f8f6f4 v[26:29], v[222:229], v[192:199], v[26:29]
	v_mfma_f32_16x16x128_f8f6f4 v[22:25], v[214:221], v[206:213], v[22:25]
	v_mfma_f32_16x16x128_f8f6f4 v[18:21], v[222:229], v[206:213], v[18:21]
	s_setprio 0
	s_add_i32 s56, s56, 2
	s_add_u32 s30, s30, 0x100
	s_addc_u32 s31, s31, 0
	s_add_u32 s54, s54, 0x100
	s_addc_u32 s55, s55, 0
	s_cmp_gt_u32 s56, 13
	s_barrier
	s_cbranch_scc0 .LBB0_202
	v_lshl_or_b32 v4, s51, 8, v171
	v_lshl_add_u32 v16, s28, 8, v1
	v_ashrrev_i32_e32 v5, 31, v4
	v_mov_b64_e32 v[2:3], s[96:97]
	v_mad_i64_i32 v[6:7], s[30:31], v16, s50, v[2:3]
	v_lshlrev_b64 v[4:5], 1, v[4:5]
	v_lshl_add_u64 v[10:11], v[6:7], 0, v[4:5]
	v_pk_mul_f32 v[8:9], v[144:145], s[8:9] op_sel_hi:[1,0]
	v_pk_mul_f32 v[6:7], v[142:143], s[8:9] op_sel_hi:[1,0]
	v_pk_mul_f32 v[12:13], v[140:141], s[8:9] op_sel_hi:[1,0]
	v_pk_mul_f32 v[14:15], v[138:139], s[8:9] op_sel_hi:[1,0]
	v_cvt_pk_bf16_f32 v6, v6, v7
	v_cvt_pk_bf16_f32 v7, v8, v9
	v_cvt_pk_bf16_f32 v8, v14, v15
	v_cvt_pk_bf16_f32 v9, v12, v13
	global_store_dwordx4 v[10:11], v[6:9], off
	v_pk_mul_f32 v[12:13], v[124:125], s[8:9] op_sel_hi:[1,0]
	v_pk_mul_f32 v[14:15], v[122:123], s[8:9] op_sel_hi:[1,0]
	v_pk_mul_f32 v[8:9], v[132:133], s[8:9] op_sel_hi:[1,0]
	v_pk_mul_f32 v[6:7], v[130:131], s[8:9] op_sel_hi:[1,0]
	s_and_b64 vcc, exec, s[0:1]
	v_cvt_pk_bf16_f32 v6, v6, v7
	v_cvt_pk_bf16_f32 v7, v8, v9
	v_cvt_pk_bf16_f32 v8, v14, v15
	v_cvt_pk_bf16_f32 v9, v12, v13
	global_store_dwordx4 v[10:11], v[6:9], off offset:256
	v_pk_mul_f32 v[12:13], v[128:129], s[8:9] op_sel_hi:[1,0]
	v_pk_mul_f32 v[14:15], v[126:127], s[8:9] op_sel_hi:[1,0]
	v_or_b32_e32 v6, 16, v16
	v_mad_i64_i32 v[6:7], s[30:31], v6, s50, v[2:3]
	v_lshl_add_u64 v[10:11], v[6:7], 0, v[4:5]
	v_pk_mul_f32 v[8:9], v[136:137], s[8:9] op_sel_hi:[1,0]
	v_pk_mul_f32 v[6:7], v[134:135], s[8:9] op_sel_hi:[1,0]
	s_mov_b32 s51, s10
	v_cvt_pk_bf16_f32 v6, v6, v7
	v_cvt_pk_bf16_f32 v7, v8, v9
	v_cvt_pk_bf16_f32 v8, v14, v15
	v_cvt_pk_bf16_f32 v9, v12, v13
	global_store_dwordx4 v[10:11], v[6:9], off
	v_pk_mul_f32 v[12:13], v[108:109], s[8:9] op_sel_hi:[1,0]
	v_pk_mul_f32 v[14:15], v[106:107], s[8:9] op_sel_hi:[1,0]
	v_pk_mul_f32 v[8:9], v[116:117], s[8:9] op_sel_hi:[1,0]
	v_pk_mul_f32 v[6:7], v[114:115], s[8:9] op_sel_hi:[1,0]
	s_mov_b32 s28, s20
	v_cvt_pk_bf16_f32 v6, v6, v7
	v_cvt_pk_bf16_f32 v7, v8, v9
	v_cvt_pk_bf16_f32 v8, v14, v15
	v_cvt_pk_bf16_f32 v9, v12, v13
	global_store_dwordx4 v[10:11], v[6:9], off offset:256
	v_pk_mul_f32 v[12:13], v[112:113], s[8:9] op_sel_hi:[1,0]
	v_pk_mul_f32 v[14:15], v[110:111], s[8:9] op_sel_hi:[1,0]
	v_or_b32_e32 v6, 32, v16
	v_mad_i64_i32 v[6:7], s[30:31], v6, s50, v[2:3]
	v_lshl_add_u64 v[10:11], v[6:7], 0, v[4:5]
	v_pk_mul_f32 v[8:9], v[120:121], s[8:9] op_sel_hi:[1,0]
	v_pk_mul_f32 v[6:7], v[118:119], s[8:9] op_sel_hi:[1,0]
	s_mov_b64 s[34:35], s[26:27]
	v_cvt_pk_bf16_f32 v6, v6, v7
	v_cvt_pk_bf16_f32 v7, v8, v9
	v_cvt_pk_bf16_f32 v8, v14, v15
	v_cvt_pk_bf16_f32 v9, v12, v13
	global_store_dwordx4 v[10:11], v[6:9], off
	v_pk_mul_f32 v[12:13], v[92:93], s[8:9] op_sel_hi:[1,0]
	v_pk_mul_f32 v[14:15], v[90:91], s[8:9] op_sel_hi:[1,0]
	v_pk_mul_f32 v[8:9], v[100:101], s[8:9] op_sel_hi:[1,0]
	v_pk_mul_f32 v[6:7], v[98:99], s[8:9] op_sel_hi:[1,0]
	s_nop 0
	v_cvt_pk_bf16_f32 v6, v6, v7
	v_cvt_pk_bf16_f32 v7, v8, v9
	v_cvt_pk_bf16_f32 v8, v14, v15
	v_cvt_pk_bf16_f32 v9, v12, v13
	global_store_dwordx4 v[10:11], v[6:9], off offset:256
	v_pk_mul_f32 v[12:13], v[96:97], s[8:9] op_sel_hi:[1,0]
	v_pk_mul_f32 v[14:15], v[94:95], s[8:9] op_sel_hi:[1,0]
	v_or_b32_e32 v6, 48, v16
	v_mad_i64_i32 v[6:7], s[30:31], v6, s50, v[2:3]
	v_lshl_add_u64 v[10:11], v[6:7], 0, v[4:5]
	v_pk_mul_f32 v[8:9], v[104:105], s[8:9] op_sel_hi:[1,0]
	v_pk_mul_f32 v[6:7], v[102:103], s[8:9] op_sel_hi:[1,0]
	s_nop 0
	v_cvt_pk_bf16_f32 v6, v6, v7
	v_cvt_pk_bf16_f32 v7, v8, v9
	v_cvt_pk_bf16_f32 v8, v14, v15
	v_cvt_pk_bf16_f32 v9, v12, v13
	global_store_dwordx4 v[10:11], v[6:9], off
	v_pk_mul_f32 v[12:13], v[84:85], s[8:9] op_sel_hi:[1,0]
	v_pk_mul_f32 v[14:15], v[82:83], s[8:9] op_sel_hi:[1,0]
	v_pk_mul_f32 v[8:9], v[88:89], s[8:9] op_sel_hi:[1,0]
	v_pk_mul_f32 v[6:7], v[86:87], s[8:9] op_sel_hi:[1,0]
	s_nop 0
	v_cvt_pk_bf16_f32 v6, v6, v7
	v_cvt_pk_bf16_f32 v7, v8, v9
	v_cvt_pk_bf16_f32 v8, v14, v15
	v_cvt_pk_bf16_f32 v9, v12, v13
	global_store_dwordx4 v[10:11], v[6:9], off offset:256
	v_pk_mul_f32 v[12:13], v[76:77], s[8:9] op_sel_hi:[1,0]
	v_pk_mul_f32 v[14:15], v[74:75], s[8:9] op_sel_hi:[1,0]
	v_add_u32_e32 v6, 0x80, v16
	v_mad_i64_i32 v[6:7], s[30:31], v6, s50, v[2:3]
	v_lshl_add_u64 v[10:11], v[6:7], 0, v[4:5]
	v_pk_mul_f32 v[8:9], v[80:81], s[8:9] op_sel_hi:[1,0]
	v_pk_mul_f32 v[6:7], v[78:79], s[8:9] op_sel_hi:[1,0]
	s_nop 0
	v_cvt_pk_bf16_f32 v6, v6, v7
	v_cvt_pk_bf16_f32 v7, v8, v9
	v_cvt_pk_bf16_f32 v8, v14, v15
	v_cvt_pk_bf16_f32 v9, v12, v13
	global_store_dwordx4 v[10:11], v[6:9], off
	v_pk_mul_f32 v[12:13], v[60:61], s[8:9] op_sel_hi:[1,0]
	v_pk_mul_f32 v[14:15], v[58:59], s[8:9] op_sel_hi:[1,0]
	v_pk_mul_f32 v[8:9], v[68:69], s[8:9] op_sel_hi:[1,0]
	v_pk_mul_f32 v[6:7], v[66:67], s[8:9] op_sel_hi:[1,0]
	s_nop 0
	v_cvt_pk_bf16_f32 v6, v6, v7
	v_cvt_pk_bf16_f32 v7, v8, v9
	v_cvt_pk_bf16_f32 v8, v14, v15
	v_cvt_pk_bf16_f32 v9, v12, v13
	global_store_dwordx4 v[10:11], v[6:9], off offset:256
	v_pk_mul_f32 v[12:13], v[64:65], s[8:9] op_sel_hi:[1,0]
	v_pk_mul_f32 v[14:15], v[62:63], s[8:9] op_sel_hi:[1,0]
	v_add_u32_e32 v6, 0x90, v16
	v_mad_i64_i32 v[6:7], s[30:31], v6, s50, v[2:3]
	v_lshl_add_u64 v[10:11], v[6:7], 0, v[4:5]
	v_pk_mul_f32 v[8:9], v[72:73], s[8:9] op_sel_hi:[1,0]
	v_pk_mul_f32 v[6:7], v[70:71], s[8:9] op_sel_hi:[1,0]
	s_nop 0
	v_cvt_pk_bf16_f32 v6, v6, v7
	v_cvt_pk_bf16_f32 v7, v8, v9
	v_cvt_pk_bf16_f32 v8, v14, v15
	v_cvt_pk_bf16_f32 v9, v12, v13
	global_store_dwordx4 v[10:11], v[6:9], off
	v_pk_mul_f32 v[12:13], v[44:45], s[8:9] op_sel_hi:[1,0]
	v_pk_mul_f32 v[14:15], v[42:43], s[8:9] op_sel_hi:[1,0]
	v_pk_mul_f32 v[8:9], v[52:53], s[8:9] op_sel_hi:[1,0]
	v_pk_mul_f32 v[6:7], v[50:51], s[8:9] op_sel_hi:[1,0]
	s_nop 0
	v_cvt_pk_bf16_f32 v6, v6, v7
	v_cvt_pk_bf16_f32 v7, v8, v9
	v_cvt_pk_bf16_f32 v8, v14, v15
	v_cvt_pk_bf16_f32 v9, v12, v13
	global_store_dwordx4 v[10:11], v[6:9], off offset:256
	v_pk_mul_f32 v[12:13], v[48:49], s[8:9] op_sel_hi:[1,0]
	v_pk_mul_f32 v[14:15], v[46:47], s[8:9] op_sel_hi:[1,0]
	v_add_u32_e32 v6, 0xa0, v16
	v_mad_i64_i32 v[6:7], s[30:31], v6, s50, v[2:3]
	v_lshl_add_u64 v[10:11], v[6:7], 0, v[4:5]
	v_pk_mul_f32 v[8:9], v[56:57], s[8:9] op_sel_hi:[1,0]
	v_pk_mul_f32 v[6:7], v[54:55], s[8:9] op_sel_hi:[1,0]
	s_nop 0
	v_cvt_pk_bf16_f32 v6, v6, v7
	v_cvt_pk_bf16_f32 v7, v8, v9
	v_cvt_pk_bf16_f32 v8, v14, v15
	v_cvt_pk_bf16_f32 v9, v12, v13
	global_store_dwordx4 v[10:11], v[6:9], off
	v_pk_mul_f32 v[12:13], v[28:29], s[8:9] op_sel_hi:[1,0]
	v_pk_mul_f32 v[14:15], v[26:27], s[8:9] op_sel_hi:[1,0]
	v_pk_mul_f32 v[8:9], v[36:37], s[8:9] op_sel_hi:[1,0]
	v_pk_mul_f32 v[6:7], v[34:35], s[8:9] op_sel_hi:[1,0]
	s_nop 0
	v_cvt_pk_bf16_f32 v6, v6, v7
	v_cvt_pk_bf16_f32 v7, v8, v9
	v_cvt_pk_bf16_f32 v8, v14, v15
	v_cvt_pk_bf16_f32 v9, v12, v13
	global_store_dwordx4 v[10:11], v[6:9], off offset:256
	v_pk_mul_f32 v[10:11], v[30:31], s[8:9] op_sel_hi:[1,0]
	s_nop 0
	v_add_u32_e32 v6, 0xb0, v16
	v_mad_i64_i32 v[2:3], s[30:31], v6, s50, v[2:3]
	v_lshl_add_u64 v[6:7], v[2:3], 0, v[4:5]
	v_pk_mul_f32 v[4:5], v[40:41], s[8:9] op_sel_hi:[1,0]
	v_pk_mul_f32 v[2:3], v[38:39], s[8:9] op_sel_hi:[1,0]
	v_pk_mul_f32 v[8:9], v[32:33], s[8:9] op_sel_hi:[1,0]
	v_cvt_pk_bf16_f32 v2, v2, v3
	v_cvt_pk_bf16_f32 v3, v4, v5
	v_cvt_pk_bf16_f32 v4, v10, v11
	v_cvt_pk_bf16_f32 v5, v8, v9
	global_store_dwordx4 v[6:7], v[2:5], off
	v_pk_mul_f32 v[8:9], v[20:21], s[8:9] op_sel_hi:[1,0]
	v_pk_mul_f32 v[10:11], v[18:19], s[8:9] op_sel_hi:[1,0]
	v_pk_mul_f32 v[4:5], v[24:25], s[8:9] op_sel_hi:[1,0]
	v_pk_mul_f32 v[2:3], v[22:23], s[8:9] op_sel_hi:[1,0]
	s_mov_b64 s[30:31], s[22:23]
	v_cvt_pk_bf16_f32 v2, v2, v3
	v_cvt_pk_bf16_f32 v3, v4, v5
	v_cvt_pk_bf16_f32 v4, v10, v11
	v_cvt_pk_bf16_f32 v5, v8, v9
	global_store_dwordx4 v[6:7], v[2:5], off offset:256
	s_cbranch_vccz .LBB0_199
	s_waitcnt vmcnt(0)
	s_cmpk_gt_u32 s2, 0xff
	s_cbranch_scc1 .LBB0_206
	s_barrier

.LBB0_495:
	ds_read_b128 v[2:5], v187
	ds_read_b128 v[6:9], v187 offset:1024
	ds_read_b128 v[10:13], v187 offset:2048
	ds_read_b128 v[14:17], v187 offset:3072
	s_add_u32 s28, s26, 0xfffc0080
	s_addc_u32 s29, s27, -1
	s_cmp_eq_u32 s52, 12
	s_cselect_b32 s31, s6, s29
	s_cselect_b32 s30, s17, s28
	s_cselect_b32 s29, s15, s51
	s_cselect_b32 s28, s49, s50
	s_add_i32 m0, s37, 0xc000
	ds_read_b128 v[192:195], v188
	ds_read_b128 v[196:199], v188 offset:1024
	ds_read_b128 v[206:209], v188 offset:2048
	ds_read_b128 v[210:213], v188 offset:3072
	ds_read_b128 v[214:217], v188 offset:4096
	ds_read_b128 v[218:221], v188 offset:5120
	ds_read_b128 v[222:225], v188 offset:6144
	ds_read_b128 v[226:229], v188 offset:7168
	global_load_lds_dwordx4 v170, s[26:27]
	s_add_i32 m0, s37, 0xe000
	s_nop 0
	global_load_lds_dwordx4 v172, s[26:27]
	s_waitcnt lgkmcnt(8)
	s_barrier
	s_waitcnt lgkmcnt(0)
	s_setprio 1
	s_waitcnt lgkmcnt(0)
	v_mfma_f32_16x16x128_f8f6f4 v[142:145], v[2:9], v[192:199], v[142:145]
	v_mfma_f32_16x16x128_f8f6f4 v[138:141], v[10:17], v[192:199], v[138:141]
	v_mfma_f32_16x16x128_f8f6f4 v[126:129], v[2:9], v[206:213], v[126:129]
	v_mfma_f32_16x16x128_f8f6f4 v[122:125], v[10:17], v[206:213], v[122:125]
	v_mfma_f32_16x16x128_f8f6f4 v[110:113], v[2:9], v[214:221], v[110:113]
	v_mfma_f32_16x16x128_f8f6f4 v[106:109], v[10:17], v[214:221], v[106:109]
	v_mfma_f32_16x16x128_f8f6f4 v[94:97], v[2:9], v[222:229], v[94:97]
	v_mfma_f32_16x16x128_f8f6f4 v[90:93], v[10:17], v[222:229], v[90:93]
	s_setprio 0
	s_barrier
	s_add_i32 s53, s46, s34
	s_mov_b32 m0, s53
	ds_read_b128 v[230:233], v190
	ds_read_b128 v[234:237], v190 offset:1024
	ds_read_b128 v[238:241], v190 offset:2048
	ds_read_b128 v[242:245], v190 offset:3072
	global_load_lds_dwordx4 v150, s[28:29]
	s_add_i32 m0, s53, 0x2000
	s_nop 0
	global_load_lds_dwordx4 v146, s[28:29]
	s_barrier
	s_waitcnt lgkmcnt(0)
	s_setprio 1
	s_waitcnt lgkmcnt(0)
	v_mfma_f32_16x16x128_f8f6f4 v[134:137], v[230:237], v[192:199], v[134:137]
	v_mfma_f32_16x16x128_f8f6f4 v[130:133], v[238:245], v[192:199], v[130:133]
	v_mfma_f32_16x16x128_f8f6f4 v[118:121], v[230:237], v[206:213], v[118:121]
	v_mfma_f32_16x16x128_f8f6f4 v[114:117], v[238:245], v[206:213], v[114:117]
	v_mfma_f32_16x16x128_f8f6f4 v[102:105], v[230:237], v[214:221], v[102:105]
	v_mfma_f32_16x16x128_f8f6f4 v[98:101], v[238:245], v[214:221], v[98:101]
	v_mfma_f32_16x16x128_f8f6f4 v[86:89], v[230:237], v[222:229], v[86:89]
	v_mfma_f32_16x16x128_f8f6f4 v[82:85], v[238:245], v[222:229], v[82:85]
	s_setprio 0
	s_mov_b32 m0, s37
	s_add_u32 s56, s30, 0x80
	s_addc_u32 s57, s31, 0
	s_barrier
	ds_read_b128 v[192:195], v188 offset:16384
	ds_read_b128 v[196:199], v188 offset:17408
	ds_read_b128 v[206:209], v188 offset:18432
	ds_read_b128 v[210:213], v188 offset:19456
	ds_read_b128 v[214:217], v188 offset:20480
	ds_read_b128 v[218:221], v188 offset:21504
	ds_read_b128 v[222:225], v188 offset:22528
	ds_read_b128 v[226:229], v188 offset:23552
	global_load_lds_dwordx4 v152, s[30:31]
	s_mov_b32 m0, s38
	s_nop 0
	global_load_lds_dwordx4 v148, s[30:31]
	s_barrier
	s_waitcnt lgkmcnt(0)
	s_setprio 1
	s_waitcnt lgkmcnt(0)
	v_mfma_f32_16x16x128_f8f6f4 v[78:81], v[2:9], v[192:199], v[78:81]
	v_mfma_f32_16x16x128_f8f6f4 v[74:77], v[10:17], v[192:199], v[74:77]
	v_mfma_f32_16x16x128_f8f6f4 v[62:65], v[2:9], v[206:213], v[62:65]
	v_mfma_f32_16x16x128_f8f6f4 v[58:61], v[10:17], v[206:213], v[58:61]
	v_mfma_f32_16x16x128_f8f6f4 v[46:49], v[2:9], v[214:221], v[46:49]
	v_mfma_f32_16x16x128_f8f6f4 v[42:45], v[10:17], v[214:221], v[42:45]
	v_mfma_f32_16x16x128_f8f6f4 v[30:33], v[2:9], v[222:229], v[30:33]
	v_mfma_f32_16x16x128_f8f6f4 v[26:29], v[10:17], v[222:229], v[26:29]
	s_setprio 0
	s_barrier
	s_add_u32 s54, s28, 0x40000
	s_addc_u32 s55, s29, 0
	s_add_i32 s53, s47, s34
	s_mov_b32 m0, s53
	s_nop 0
	global_load_lds_dwordx4 v150, s[54:55]
	s_add_i32 m0, s53, 0x2000
	s_nop 0
	global_load_lds_dwordx4 v146, s[54:55]
	s_waitcnt vmcnt(6)
	s_barrier
	s_setprio 1
	v_mfma_f32_16x16x128_f8f6f4 v[70:73], v[230:237], v[192:199], v[70:73]
	v_mfma_f32_16x16x128_f8f6f4 v[66:69], v[238:245], v[192:199], v[66:69]
	v_mfma_f32_16x16x128_f8f6f4 v[54:57], v[230:237], v[206:213], v[54:57]
	v_mfma_f32_16x16x128_f8f6f4 v[50:53], v[238:245], v[206:213], v[50:53]
	v_mfma_f32_16x16x128_f8f6f4 v[38:41], v[230:237], v[214:221], v[38:41]
	v_mfma_f32_16x16x128_f8f6f4 v[34:37], v[238:245], v[214:221], v[34:37]
	v_mfma_f32_16x16x128_f8f6f4 v[22:25], v[230:237], v[222:229], v[22:25]
	v_mfma_f32_16x16x128_f8f6f4 v[18:21], v[238:245], v[222:229], v[18:21]
	s_setprio 0
	s_add_i32 s53, 0, 0x18000
	v_add_u32_e32 v14, s53, v1
	s_barrier
	ds_read_b128 v[2:5], v14
	ds_read_b128 v[6:9], v14 offset:1024
	ds_read_b128 v[10:13], v14 offset:2048
	ds_read_b128 v[14:17], v14 offset:3072
	s_add_u32 s30, s30, 0x40000
	s_addc_u32 s31, s31, 0
	s_mov_b32 m0, s39
	ds_read_b128 v[192:195], v188 offset:32768
	ds_read_b128 v[196:199], v188 offset:33792
	ds_read_b128 v[206:209], v188 offset:34816
	ds_read_b128 v[210:213], v188 offset:35840
	ds_read_b128 v[214:217], v188 offset:36864
	ds_read_b128 v[218:221], v188 offset:37888
	ds_read_b128 v[222:225], v188 offset:38912
	ds_read_b128 v[226:229], v188 offset:39936
	global_load_lds_dwordx4 v152, s[30:31]
	s_mov_b32 m0, s40
	s_nop 0
	global_load_lds_dwordx4 v148, s[30:31]
	s_waitcnt lgkmcnt(8)
	s_barrier
	s_waitcnt lgkmcnt(0)
	s_setprio 1
	s_waitcnt lgkmcnt(0)
	v_mfma_f32_16x16x128_f8f6f4 v[142:145], v[2:9], v[192:199], v[142:145]
	v_mfma_f32_16x16x128_f8f6f4 v[138:141], v[10:17], v[192:199], v[138:141]
	v_mfma_f32_16x16x128_f8f6f4 v[126:129], v[2:9], v[206:213], v[126:129]
	v_mfma_f32_16x16x128_f8f6f4 v[122:125], v[10:17], v[206:213], v[122:125]
	v_mfma_f32_16x16x128_f8f6f4 v[110:113], v[2:9], v[214:221], v[110:113]
	v_mfma_f32_16x16x128_f8f6f4 v[106:109], v[10:17], v[214:221], v[106:109]
	v_mfma_f32_16x16x128_f8f6f4 v[94:97], v[2:9], v[222:229], v[94:97]
	v_mfma_f32_16x16x128_f8f6f4 v[90:93], v[10:17], v[222:229], v[90:93]
	s_setprio 0
	s_barrier
	s_add_i32 s30, 0, 0x1c000
	s_add_i32 s31, s53, s34
	v_add_u32_e32 v191, s30, v1
	s_add_u32 s54, s28, 0x80
	s_addc_u32 s55, s29, 0
	s_mov_b32 m0, s31
	ds_read_b128 v[230:233], v191
	ds_read_b128 v[234:237], v191 offset:1024
	ds_read_b128 v[238:241], v191 offset:2048
	ds_read_b128 v[242:245], v191 offset:3072
	global_load_lds_dwordx4 v150, s[54:55]
	s_add_i32 m0, s31, 0x2000
	s_nop 0
	global_load_lds_dwordx4 v146, s[54:55]
	s_barrier
	s_waitcnt lgkmcnt(0)
	s_setprio 1
	s_waitcnt lgkmcnt(0)
	v_mfma_f32_16x16x128_f8f6f4 v[134:137], v[230:237], v[192:199], v[134:137]
	v_mfma_f32_16x16x128_f8f6f4 v[130:133], v[238:245], v[192:199], v[130:133]
	v_mfma_f32_16x16x128_f8f6f4 v[118:121], v[230:237], v[206:213], v[118:121]
	v_mfma_f32_16x16x128_f8f6f4 v[114:117], v[238:245], v[206:213], v[114:117]
	v_mfma_f32_16x16x128_f8f6f4 v[102:105], v[230:237], v[214:221], v[102:105]
	v_mfma_f32_16x16x128_f8f6f4 v[98:101], v[238:245], v[214:221], v[98:101]
	v_mfma_f32_16x16x128_f8f6f4 v[86:89], v[230:237], v[222:229], v[86:89]
	v_mfma_f32_16x16x128_f8f6f4 v[82:85], v[238:245], v[222:229], v[82:85]
	s_setprio 0
	s_mov_b32 m0, s43
	s_barrier
	ds_read_b128 v[192:195], v188 offset:49152
	ds_read_b128 v[196:199], v188 offset:50176
	ds_read_b128 v[206:209], v188 offset:51200
	ds_read_b128 v[210:213], v188 offset:52224
	ds_read_b128 v[214:217], v188 offset:53248
	ds_read_b128 v[218:221], v188 offset:54272
	ds_read_b128 v[222:225], v188 offset:55296
	ds_read_b128 v[226:229], v188 offset:56320
	global_load_lds_dwordx4 v152, s[56:57]
	s_mov_b32 m0, s44
	s_nop 0
	global_load_lds_dwordx4 v148, s[56:57]
	s_barrier
	s_waitcnt lgkmcnt(0)
	s_setprio 1
	s_waitcnt lgkmcnt(0)
	v_mfma_f32_16x16x128_f8f6f4 v[78:81], v[2:9], v[192:199], v[78:81]
	v_mfma_f32_16x16x128_f8f6f4 v[74:77], v[10:17], v[192:199], v[74:77]
	v_mfma_f32_16x16x128_f8f6f4 v[62:65], v[2:9], v[206:213], v[62:65]
	v_mfma_f32_16x16x128_f8f6f4 v[58:61], v[10:17], v[206:213], v[58:61]
	v_mfma_f32_16x16x128_f8f6f4 v[46:49], v[2:9], v[214:221], v[46:49]
	v_mfma_f32_16x16x128_f8f6f4 v[42:45], v[10:17], v[214:221], v[42:45]
	v_mfma_f32_16x16x128_f8f6f4 v[30:33], v[2:9], v[222:229], v[30:33]
	v_mfma_f32_16x16x128_f8f6f4 v[26:29], v[10:17], v[222:229], v[26:29]
	s_setprio 0
	s_barrier
	s_add_u32 s28, s28, 0x40080
	s_addc_u32 s29, s29, 0
	s_add_i32 s30, s30, s34
	s_mov_b32 m0, s30
	s_nop 0
	global_load_lds_dwordx4 v150, s[28:29]
	s_add_i32 m0, s30, 0x2000
	s_nop 0
	global_load_lds_dwordx4 v146, s[28:29]
	s_waitcnt vmcnt(6)
	s_barrier
	s_setprio 1
	v_mfma_f32_16x16x128_f8f6f4 v[70:73], v[230:237], v[192:199], v[70:73]
	v_mfma_f32_16x16x128_f8f6f4 v[66:69], v[238:245], v[192:199], v[66:69]
	v_mfma_f32_16x16x128_f8f6f4 v[54:57], v[230:237], v[206:213], v[54:57]
	v_mfma_f32_16x16x128_f8f6f4 v[50:53], v[238:245], v[206:213], v[50:53]
	v_mfma_f32_16x16x128_f8f6f4 v[38:41], v[230:237], v[214:221], v[38:41]
	v_mfma_f32_16x16x128_f8f6f4 v[34:37], v[238:245], v[214:221], v[34:37]
	v_mfma_f32_16x16x128_f8f6f4 v[22:25], v[230:237], v[222:229], v[22:25]
	v_mfma_f32_16x16x128_f8f6f4 v[18:21], v[238:245], v[222:229], v[18:21]
	s_setprio 0
	s_add_i32 s52, s52, 2
	s_add_u32 s26, s26, 0x100
	s_addc_u32 s27, s27, 0
	s_add_u32 s50, s50, 0x100
	s_addc_u32 s51, s51, 0
	s_cmp_gt_u32 s52, 13
	s_barrier
	s_cbranch_scc0 .LBB0_495
	s_lshl_b32 s28, s22, 8
	s_cmpk_gt_i32 s22, 0x7f
	s_mov_b64 s[30:31], -1
	s_cbranch_scc0 .LBB0_498
	s_add_i32 s6, s28, 0xffff8000
	v_readlane_b32 s60, v254, 18
	s_lshl_b64 s[26:27], s[6:7], 13
	v_readlane_b32 s64, v254, 22
	v_readlane_b32 s65, v254, 23
	s_add_u32 s26, s64, s26
	v_readlane_b32 s61, v254, 19
	v_readlane_b32 s62, v254, 20
	v_readlane_b32 s63, v254, 21
	v_readlane_b32 s66, v254, 24
	v_readlane_b32 s67, v254, 25
	v_readlane_b32 s68, v254, 26
	v_readlane_b32 s69, v254, 27
	v_readlane_b32 s70, v254, 28
	v_readlane_b32 s71, v254, 29
	v_readlane_b32 s72, v254, 30
	v_readlane_b32 s73, v254, 31
	v_readlane_b32 s74, v254, 32
	v_readlane_b32 s75, v254, 33
	s_addc_u32 s27, s65, s27
	s_mov_b32 s29, s7
	s_mov_b64 s[30:31], 0

.LBB0_820:
	ds_read_b128 v[2:5], v176
	ds_read_b128 v[6:9], v176 offset:1024
	ds_read_b128 v[10:13], v176 offset:2048
	ds_read_b128 v[14:17], v176 offset:3072
	s_add_u32 s26, s24, 0xfffc0080
	s_addc_u32 s27, s25, -1
	s_cmp_eq_u32 s60, 12
	s_cselect_b32 s29, s17, s27
	s_cselect_b32 s28, s23, s26
	s_cselect_b32 s27, s15, s59
	s_cselect_b32 s26, s56, s57
	s_add_i32 m0, s36, 0xc000
	ds_read_b128 v[190:193], v177
	ds_read_b128 v[194:197], v177 offset:1024
	ds_read_b128 v[214:217], v177 offset:2048
	ds_read_b128 v[218:221], v177 offset:3072
	ds_read_b128 v[222:225], v177 offset:4096
	ds_read_b128 v[226:229], v177 offset:5120
	ds_read_b128 v[230:233], v177 offset:6144
	ds_read_b128 v[234:237], v177 offset:7168
	global_load_lds_dwordx4 v158, s[24:25]
	s_add_i32 m0, s36, 0xe000
	s_nop 0
	global_load_lds_dwordx4 v160, s[24:25]
	s_waitcnt lgkmcnt(8)
	s_barrier
	s_waitcnt lgkmcnt(0)
	s_setprio 1
	s_waitcnt lgkmcnt(0)
	v_mfma_f32_16x16x128_f8f6f4 v[142:145], v[2:9], v[190:197], v[142:145]
	v_mfma_f32_16x16x128_f8f6f4 v[138:141], v[10:17], v[190:197], v[138:141]
	v_mfma_f32_16x16x128_f8f6f4 v[126:129], v[2:9], v[214:221], v[126:129]
	v_mfma_f32_16x16x128_f8f6f4 v[122:125], v[10:17], v[214:221], v[122:125]
	v_mfma_f32_16x16x128_f8f6f4 v[110:113], v[2:9], v[222:229], v[110:113]
	v_mfma_f32_16x16x128_f8f6f4 v[106:109], v[10:17], v[222:229], v[106:109]
	v_mfma_f32_16x16x128_f8f6f4 v[94:97], v[2:9], v[230:237], v[94:97]
	v_mfma_f32_16x16x128_f8f6f4 v[90:93], v[10:17], v[230:237], v[90:93]
	s_setprio 0
	s_barrier
	s_add_i32 s61, s48, s33
	s_add_u32 s66, s26, 0x80
	s_addc_u32 s67, s27, 0
	s_mov_b32 m0, s61
	ds_read_b128 v[238:241], v179
	ds_read_b128 v[242:245], v179 offset:1024
	ds_read_b128 v[246:249], v179 offset:2048
	ds_read_b128 v[250:253], v179 offset:3072
	global_load_lds_dwordx4 v150, s[26:27]
	s_add_i32 m0, s61, 0x2000
	s_nop 0
	global_load_lds_dwordx4 v146, s[26:27]
	s_barrier
	s_waitcnt lgkmcnt(0)
	s_setprio 1
	s_waitcnt lgkmcnt(0)
	v_mfma_f32_16x16x128_f8f6f4 v[134:137], v[238:245], v[190:197], v[134:137]
	v_mfma_f32_16x16x128_f8f6f4 v[130:133], v[246:253], v[190:197], v[130:133]
	v_mfma_f32_16x16x128_f8f6f4 v[118:121], v[238:245], v[214:221], v[118:121]
	v_mfma_f32_16x16x128_f8f6f4 v[114:117], v[246:253], v[214:221], v[114:117]
	v_mfma_f32_16x16x128_f8f6f4 v[102:105], v[238:245], v[222:229], v[102:105]
	v_mfma_f32_16x16x128_f8f6f4 v[98:101], v[246:253], v[222:229], v[98:101]
	v_mfma_f32_16x16x128_f8f6f4 v[86:89], v[238:245], v[230:237], v[86:89]
	v_mfma_f32_16x16x128_f8f6f4 v[82:85], v[246:253], v[230:237], v[82:85]
	s_setprio 0
	s_mov_b32 m0, s36
	s_add_u32 s68, s28, 0x80
	s_addc_u32 s69, s29, 0
	s_barrier
	ds_read_b128 v[190:193], v177 offset:16384
	ds_read_b128 v[194:197], v177 offset:17408
	ds_read_b128 v[214:217], v177 offset:18432
	ds_read_b128 v[218:221], v177 offset:19456
	ds_read_b128 v[222:225], v177 offset:20480
	ds_read_b128 v[226:229], v177 offset:21504
	ds_read_b128 v[230:233], v177 offset:22528
	ds_read_b128 v[234:237], v177 offset:23552
	global_load_lds_dwordx4 v152, s[28:29]
	s_mov_b32 m0, s37
	s_nop 0
	global_load_lds_dwordx4 v148, s[28:29]
	s_barrier
	s_waitcnt lgkmcnt(0)
	s_setprio 1
	s_waitcnt lgkmcnt(0)
	v_mfma_f32_16x16x128_f8f6f4 v[78:81], v[2:9], v[190:197], v[78:81]
	v_mfma_f32_16x16x128_f8f6f4 v[74:77], v[10:17], v[190:197], v[74:77]
	v_mfma_f32_16x16x128_f8f6f4 v[62:65], v[2:9], v[214:221], v[62:65]
	v_mfma_f32_16x16x128_f8f6f4 v[58:61], v[10:17], v[214:221], v[58:61]
	v_mfma_f32_16x16x128_f8f6f4 v[50:53], v[2:9], v[222:229], v[50:53]
	v_mfma_f32_16x16x128_f8f6f4 v[42:45], v[10:17], v[222:229], v[42:45]
	v_mfma_f32_16x16x128_f8f6f4 v[34:37], v[2:9], v[230:237], v[34:37]
	v_mfma_f32_16x16x128_f8f6f4 v[26:29], v[10:17], v[230:237], v[26:29]
	s_setprio 0
	s_barrier
	s_add_u32 s62, s26, 0x40000
	s_addc_u32 s63, s27, 0
	s_add_i32 s61, s49, s33
	s_mov_b32 m0, s61
	s_nop 0
	global_load_lds_dwordx4 v150, s[62:63]
	s_add_i32 m0, s61, 0x2000
	s_nop 0
	global_load_lds_dwordx4 v146, s[62:63]
	s_waitcnt vmcnt(6)
	s_barrier
	s_setprio 1
	v_mfma_f32_16x16x128_f8f6f4 v[70:73], v[238:245], v[190:197], v[70:73]
	v_mfma_f32_16x16x128_f8f6f4 v[66:69], v[246:253], v[190:197], v[66:69]
	v_mfma_f32_16x16x128_f8f6f4 v[54:57], v[238:245], v[214:221], v[54:57]
	v_mfma_f32_16x16x128_f8f6f4 v[46:49], v[246:253], v[214:221], v[46:49]
	v_mfma_f32_16x16x128_f8f6f4 v[38:41], v[238:245], v[222:229], v[38:41]
	v_mfma_f32_16x16x128_f8f6f4 v[30:33], v[246:253], v[222:229], v[30:33]
	v_mfma_f32_16x16x128_f8f6f4 v[22:25], v[238:245], v[230:237], v[22:25]
	v_mfma_f32_16x16x128_f8f6f4 v[18:21], v[246:253], v[230:237], v[18:21]
	s_setprio 0
	s_add_i32 s61, 0, 0x18000
	v_add_u32_e32 v14, s61, v175
	s_barrier
	ds_read_b128 v[2:5], v14
	ds_read_b128 v[6:9], v14 offset:1024
	ds_read_b128 v[10:13], v14 offset:2048
	ds_read_b128 v[14:17], v14 offset:3072
	s_add_u32 s28, s28, 0x40000
	s_addc_u32 s29, s29, 0
	s_mov_b32 m0, s38
	ds_read_b128 v[190:193], v177 offset:32768
	ds_read_b128 v[194:197], v177 offset:33792
	ds_read_b128 v[214:217], v177 offset:34816
	ds_read_b128 v[218:221], v177 offset:35840
	ds_read_b128 v[222:225], v177 offset:36864
	ds_read_b128 v[226:229], v177 offset:37888
	ds_read_b128 v[230:233], v177 offset:38912
	ds_read_b128 v[234:237], v177 offset:39936
	global_load_lds_dwordx4 v152, s[28:29]
	s_mov_b32 m0, s39
	s_nop 0
	global_load_lds_dwordx4 v148, s[28:29]
	s_waitcnt lgkmcnt(8)
	s_barrier
	s_waitcnt lgkmcnt(0)
	s_setprio 1
	s_waitcnt lgkmcnt(0)
	v_mfma_f32_16x16x128_f8f6f4 v[142:145], v[2:9], v[190:197], v[142:145]
	v_mfma_f32_16x16x128_f8f6f4 v[138:141], v[10:17], v[190:197], v[138:141]
	v_mfma_f32_16x16x128_f8f6f4 v[126:129], v[2:9], v[214:221], v[126:129]
	v_mfma_f32_16x16x128_f8f6f4 v[122:125], v[10:17], v[214:221], v[122:125]
	v_mfma_f32_16x16x128_f8f6f4 v[110:113], v[2:9], v[222:229], v[110:113]
	v_mfma_f32_16x16x128_f8f6f4 v[106:109], v[10:17], v[222:229], v[106:109]
	v_mfma_f32_16x16x128_f8f6f4 v[94:97], v[2:9], v[230:237], v[94:97]
	v_mfma_f32_16x16x128_f8f6f4 v[90:93], v[10:17], v[230:237], v[90:93]
	s_setprio 0
	s_barrier
	s_add_i32 s28, 0, 0x1c000
	s_add_i32 s29, s61, s33
	v_add_u32_e32 v154, s28, v175
	s_mov_b32 m0, s29
	ds_read_b128 v[238:241], v154
	ds_read_b128 v[242:245], v154 offset:1024
	ds_read_b128 v[246:249], v154 offset:2048
	ds_read_b128 v[250:253], v154 offset:3072
	global_load_lds_dwordx4 v150, s[66:67]
	s_add_i32 m0, s29, 0x2000
	s_nop 0
	global_load_lds_dwordx4 v146, s[66:67]
	s_barrier
	s_waitcnt lgkmcnt(0)
	s_setprio 1
	s_waitcnt lgkmcnt(0)
	v_mfma_f32_16x16x128_f8f6f4 v[134:137], v[238:245], v[190:197], v[134:137]
	v_mfma_f32_16x16x128_f8f6f4 v[130:133], v[246:253], v[190:197], v[130:133]
	v_mfma_f32_16x16x128_f8f6f4 v[118:121], v[238:245], v[214:221], v[118:121]
	v_mfma_f32_16x16x128_f8f6f4 v[114:117], v[246:253], v[214:221], v[114:117]
	v_mfma_f32_16x16x128_f8f6f4 v[102:105], v[238:245], v[222:229], v[102:105]
	v_mfma_f32_16x16x128_f8f6f4 v[98:101], v[246:253], v[222:229], v[98:101]
	v_mfma_f32_16x16x128_f8f6f4 v[86:89], v[238:245], v[230:237], v[86:89]
	v_mfma_f32_16x16x128_f8f6f4 v[82:85], v[246:253], v[230:237], v[82:85]
	s_setprio 0
	s_mov_b32 m0, s45
	s_barrier
	ds_read_b128 v[190:193], v177 offset:49152
	ds_read_b128 v[194:197], v177 offset:50176
	ds_read_b128 v[214:217], v177 offset:51200
	ds_read_b128 v[218:221], v177 offset:52224
	ds_read_b128 v[222:225], v177 offset:53248
	ds_read_b128 v[226:229], v177 offset:54272
	ds_read_b128 v[230:233], v177 offset:55296
	ds_read_b128 v[234:237], v177 offset:56320
	global_load_lds_dwordx4 v152, s[68:69]
	s_mov_b32 m0, s46
	s_nop 0
	global_load_lds_dwordx4 v148, s[68:69]
	s_barrier
	s_waitcnt lgkmcnt(0)
	s_setprio 1
	s_waitcnt lgkmcnt(0)
	v_mfma_f32_16x16x128_f8f6f4 v[78:81], v[2:9], v[190:197], v[78:81]
	v_mfma_f32_16x16x128_f8f6f4 v[74:77], v[10:17], v[190:197], v[74:77]
	v_mfma_f32_16x16x128_f8f6f4 v[62:65], v[2:9], v[214:221], v[62:65]
	v_mfma_f32_16x16x128_f8f6f4 v[58:61], v[10:17], v[214:221], v[58:61]
	v_mfma_f32_16x16x128_f8f6f4 v[50:53], v[2:9], v[222:229], v[50:53]
	v_mfma_f32_16x16x128_f8f6f4 v[42:45], v[10:17], v[222:229], v[42:45]
	v_mfma_f32_16x16x128_f8f6f4 v[34:37], v[2:9], v[230:237], v[34:37]
	v_mfma_f32_16x16x128_f8f6f4 v[26:29], v[10:17], v[230:237], v[26:29]
	s_setprio 0
	s_barrier
	s_add_u32 s26, s26, 0x40080
	s_addc_u32 s27, s27, 0
	s_add_i32 s28, s28, s33
	s_mov_b32 m0, s28
	s_nop 0
	global_load_lds_dwordx4 v150, s[26:27]
	s_add_i32 m0, s28, 0x2000
	s_nop 0
	global_load_lds_dwordx4 v146, s[26:27]
	s_waitcnt vmcnt(6)
	s_barrier
	s_setprio 1
	v_mfma_f32_16x16x128_f8f6f4 v[70:73], v[238:245], v[190:197], v[70:73]
	v_mfma_f32_16x16x128_f8f6f4 v[66:69], v[246:253], v[190:197], v[66:69]
	v_mfma_f32_16x16x128_f8f6f4 v[54:57], v[238:245], v[214:221], v[54:57]
	v_mfma_f32_16x16x128_f8f6f4 v[46:49], v[246:253], v[214:221], v[46:49]
	v_mfma_f32_16x16x128_f8f6f4 v[38:41], v[238:245], v[222:229], v[38:41]
	v_mfma_f32_16x16x128_f8f6f4 v[30:33], v[246:253], v[222:229], v[30:33]
	v_mfma_f32_16x16x128_f8f6f4 v[22:25], v[238:245], v[230:237], v[22:25]
	v_mfma_f32_16x16x128_f8f6f4 v[18:21], v[246:253], v[230:237], v[18:21]
	s_setprio 0
	s_add_i32 s60, s60, 2
	s_add_u32 s24, s24, 0x100
	s_addc_u32 s25, s25, 0
	s_add_u32 s57, s57, 0x100
	s_addc_u32 s59, s59, 0
	s_cmp_gt_u32 s60, 13
	s_barrier
	s_cbranch_scc0 .LBB0_820
	v_lshl_add_u32 v10, s22, 8, v174
	s_add_i32 s15, s55, -4
	s_mov_b64 s[22:23], -1
	s_cmp_lt_u32 s15, 8
	v_or_b32_e32 v8, 16, v10
	v_or_b32_e32 v4, 32, v10
	v_or_b32_e32 v2, 48, v10
	s_cbranch_scc1 .LBB0_823
	s_lshl_b32 s22, s55, 8
	s_ashr_i32 s23, s22, 31
	v_mov_b64_e32 v[6:7], s[96:97]
	v_mad_i64_i32 v[12:13], s[24:25], v10, s50, v[6:7]
	s_lshl_b64 s[22:23], s[22:23], 1
	v_lshl_add_u64 v[12:13], v[12:13], 0, s[22:23]
	v_lshlrev_b32_e32 v154, 1, v156
	v_lshl_add_u64 v[16:17], v[12:13], 0, v[154:155]
	v_pk_mul_f32 v[14:15], v[144:145], s[8:9] op_sel_hi:[1,0]
	v_pk_mul_f32 v[12:13], v[142:143], s[8:9] op_sel_hi:[1,0]
	v_pk_mul_f32 v[166:167], v[140:141], s[8:9] op_sel_hi:[1,0]
	v_pk_mul_f32 v[168:169], v[138:139], s[8:9] op_sel_hi:[1,0]
	v_cvt_pk_bf16_f32 v12, v12, v13
	v_cvt_pk_bf16_f32 v13, v14, v15
	v_cvt_pk_bf16_f32 v14, v168, v169
	v_cvt_pk_bf16_f32 v15, v166, v167
	global_store_dwordx4 v[16:17], v[12:15], off
	v_pk_mul_f32 v[166:167], v[132:133], s[8:9] op_sel_hi:[1,0]
	v_pk_mul_f32 v[168:169], v[130:131], s[8:9] op_sel_hi:[1,0]
	v_pk_mul_f32 v[14:15], v[136:137], s[8:9] op_sel_hi:[1,0]
	v_pk_mul_f32 v[12:13], v[134:135], s[8:9] op_sel_hi:[1,0]
	v_add_u32_e32 v3, 0x80, v10
	v_cvt_pk_bf16_f32 v12, v12, v13
	v_cvt_pk_bf16_f32 v13, v14, v15
	v_cvt_pk_bf16_f32 v14, v168, v169
	v_cvt_pk_bf16_f32 v15, v166, v167
	global_store_dwordx4 v[16:17], v[12:15], off offset:256
	v_pk_mul_f32 v[166:167], v[124:125], s[8:9] op_sel_hi:[1,0]
	v_pk_mul_f32 v[168:169], v[122:123], s[8:9] op_sel_hi:[1,0]
	v_mad_i64_i32 v[12:13], s[24:25], v8, s50, v[6:7]
	v_lshl_add_u64 v[12:13], v[12:13], 0, s[22:23]
	v_lshl_add_u64 v[16:17], v[12:13], 0, v[154:155]
	v_pk_mul_f32 v[14:15], v[128:129], s[8:9] op_sel_hi:[1,0]
	v_pk_mul_f32 v[12:13], v[126:127], s[8:9] op_sel_hi:[1,0]
	s_nop 0
	v_cvt_pk_bf16_f32 v12, v12, v13
	v_cvt_pk_bf16_f32 v13, v14, v15
	v_cvt_pk_bf16_f32 v14, v168, v169
	v_cvt_pk_bf16_f32 v15, v166, v167
	global_store_dwordx4 v[16:17], v[12:15], off
	v_pk_mul_f32 v[166:167], v[116:117], s[8:9] op_sel_hi:[1,0]
	v_pk_mul_f32 v[168:169], v[114:115], s[8:9] op_sel_hi:[1,0]
	v_pk_mul_f32 v[14:15], v[120:121], s[8:9] op_sel_hi:[1,0]
	v_pk_mul_f32 v[12:13], v[118:119], s[8:9] op_sel_hi:[1,0]
	s_nop 0
	v_cvt_pk_bf16_f32 v12, v12, v13
	v_cvt_pk_bf16_f32 v13, v14, v15
	v_cvt_pk_bf16_f32 v14, v168, v169
	v_cvt_pk_bf16_f32 v15, v166, v167
	global_store_dwordx4 v[16:17], v[12:15], off offset:256
	v_pk_mul_f32 v[166:167], v[108:109], s[8:9] op_sel_hi:[1,0]
	v_pk_mul_f32 v[168:169], v[106:107], s[8:9] op_sel_hi:[1,0]
	v_mad_i64_i32 v[12:13], s[24:25], v4, s50, v[6:7]
	v_lshl_add_u64 v[12:13], v[12:13], 0, s[22:23]
	v_lshl_add_u64 v[16:17], v[12:13], 0, v[154:155]
	v_pk_mul_f32 v[14:15], v[112:113], s[8:9] op_sel_hi:[1,0]
	v_pk_mul_f32 v[12:13], v[110:111], s[8:9] op_sel_hi:[1,0]
	s_nop 0
	v_cvt_pk_bf16_f32 v12, v12, v13
	v_cvt_pk_bf16_f32 v13, v14, v15
	v_cvt_pk_bf16_f32 v14, v168, v169
	v_cvt_pk_bf16_f32 v15, v166, v167
	global_store_dwordx4 v[16:17], v[12:15], off
	v_pk_mul_f32 v[166:167], v[100:101], s[8:9] op_sel_hi:[1,0]
	v_pk_mul_f32 v[168:169], v[98:99], s[8:9] op_sel_hi:[1,0]
	v_pk_mul_f32 v[14:15], v[104:105], s[8:9] op_sel_hi:[1,0]
	v_pk_mul_f32 v[12:13], v[102:103], s[8:9] op_sel_hi:[1,0]
	s_nop 0
	v_cvt_pk_bf16_f32 v12, v12, v13
	v_cvt_pk_bf16_f32 v13, v14, v15
	v_cvt_pk_bf16_f32 v14, v168, v169
	v_cvt_pk_bf16_f32 v15, v166, v167
	global_store_dwordx4 v[16:17], v[12:15], off offset:256
	v_pk_mul_f32 v[166:167], v[92:93], s[8:9] op_sel_hi:[1,0]
	v_pk_mul_f32 v[168:169], v[90:91], s[8:9] op_sel_hi:[1,0]
	v_mad_i64_i32 v[12:13], s[24:25], v2, s50, v[6:7]
	v_lshl_add_u64 v[12:13], v[12:13], 0, s[22:23]
	v_lshl_add_u64 v[16:17], v[12:13], 0, v[154:155]
	v_pk_mul_f32 v[14:15], v[96:97], s[8:9] op_sel_hi:[1,0]
	v_pk_mul_f32 v[12:13], v[94:95], s[8:9] op_sel_hi:[1,0]
	s_nop 0
	v_cvt_pk_bf16_f32 v12, v12, v13
	v_cvt_pk_bf16_f32 v13, v14, v15
	v_cvt_pk_bf16_f32 v14, v168, v169
	v_cvt_pk_bf16_f32 v15, v166, v167
	global_store_dwordx4 v[16:17], v[12:15], off
	v_pk_mul_f32 v[166:167], v[84:85], s[8:9] op_sel_hi:[1,0]
	v_pk_mul_f32 v[168:169], v[82:83], s[8:9] op_sel_hi:[1,0]
	v_pk_mul_f32 v[14:15], v[88:89], s[8:9] op_sel_hi:[1,0]
	v_pk_mul_f32 v[12:13], v[86:87], s[8:9] op_sel_hi:[1,0]
	s_nop 0
	v_cvt_pk_bf16_f32 v12, v12, v13
	v_cvt_pk_bf16_f32 v13, v14, v15
	v_cvt_pk_bf16_f32 v14, v168, v169
	v_cvt_pk_bf16_f32 v15, v166, v167
	global_store_dwordx4 v[16:17], v[12:15], off offset:256
	v_pk_mul_f32 v[166:167], v[76:77], s[8:9] op_sel_hi:[1,0]
	v_pk_mul_f32 v[168:169], v[74:75], s[8:9] op_sel_hi:[1,0]
	v_mad_i64_i32 v[12:13], s[24:25], v3, s50, v[6:7]
	v_lshl_add_u64 v[12:13], v[12:13], 0, s[22:23]
	v_lshl_add_u64 v[16:17], v[12:13], 0, v[154:155]
	v_pk_mul_f32 v[14:15], v[80:81], s[8:9] op_sel_hi:[1,0]
	v_pk_mul_f32 v[12:13], v[78:79], s[8:9] op_sel_hi:[1,0]
	v_add_u32_e32 v3, 0x90, v10
	v_cvt_pk_bf16_f32 v12, v12, v13
	v_cvt_pk_bf16_f32 v13, v14, v15
	v_cvt_pk_bf16_f32 v14, v168, v169
	v_cvt_pk_bf16_f32 v15, v166, v167
	global_store_dwordx4 v[16:17], v[12:15], off
	v_pk_mul_f32 v[166:167], v[68:69], s[8:9] op_sel_hi:[1,0]
	v_pk_mul_f32 v[168:169], v[66:67], s[8:9] op_sel_hi:[1,0]
	v_pk_mul_f32 v[14:15], v[72:73], s[8:9] op_sel_hi:[1,0]
	v_pk_mul_f32 v[12:13], v[70:71], s[8:9] op_sel_hi:[1,0]
	s_nop 0
	v_cvt_pk_bf16_f32 v12, v12, v13
	v_cvt_pk_bf16_f32 v13, v14, v15
	v_cvt_pk_bf16_f32 v14, v168, v169
	v_cvt_pk_bf16_f32 v15, v166, v167
	global_store_dwordx4 v[16:17], v[12:15], off offset:256
	v_pk_mul_f32 v[166:167], v[60:61], s[8:9] op_sel_hi:[1,0]
	v_pk_mul_f32 v[168:169], v[58:59], s[8:9] op_sel_hi:[1,0]
	v_mad_i64_i32 v[12:13], s[24:25], v3, s50, v[6:7]
	v_lshl_add_u64 v[12:13], v[12:13], 0, s[22:23]
	v_lshl_add_u64 v[16:17], v[12:13], 0, v[154:155]
	v_pk_mul_f32 v[14:15], v[64:65], s[8:9] op_sel_hi:[1,0]
	v_pk_mul_f32 v[12:13], v[62:63], s[8:9] op_sel_hi:[1,0]
	v_add_u32_e32 v3, 0xa0, v10
	v_cvt_pk_bf16_f32 v12, v12, v13
	v_cvt_pk_bf16_f32 v13, v14, v15
	v_cvt_pk_bf16_f32 v14, v168, v169
	v_cvt_pk_bf16_f32 v15, v166, v167
	global_store_dwordx4 v[16:17], v[12:15], off
	v_pk_mul_f32 v[166:167], v[48:49], s[8:9] op_sel_hi:[1,0]
	v_pk_mul_f32 v[168:169], v[46:47], s[8:9] op_sel_hi:[1,0]
	v_pk_mul_f32 v[14:15], v[56:57], s[8:9] op_sel_hi:[1,0]
	v_pk_mul_f32 v[12:13], v[54:55], s[8:9] op_sel_hi:[1,0]
	s_nop 0
	v_cvt_pk_bf16_f32 v12, v12, v13
	v_cvt_pk_bf16_f32 v13, v14, v15
	v_cvt_pk_bf16_f32 v14, v168, v169
	v_cvt_pk_bf16_f32 v15, v166, v167
	global_store_dwordx4 v[16:17], v[12:15], off offset:256
	v_pk_mul_f32 v[166:167], v[44:45], s[8:9] op_sel_hi:[1,0]
	v_pk_mul_f32 v[168:169], v[42:43], s[8:9] op_sel_hi:[1,0]
	v_mad_i64_i32 v[12:13], s[24:25], v3, s50, v[6:7]
	v_lshl_add_u64 v[12:13], v[12:13], 0, s[22:23]
	v_lshl_add_u64 v[16:17], v[12:13], 0, v[154:155]
	v_pk_mul_f32 v[14:15], v[52:53], s[8:9] op_sel_hi:[1,0]
	v_pk_mul_f32 v[12:13], v[50:51], s[8:9] op_sel_hi:[1,0]
	v_add_u32_e32 v3, 0xb0, v10
	v_cvt_pk_bf16_f32 v12, v12, v13
	v_cvt_pk_bf16_f32 v13, v14, v15
	v_cvt_pk_bf16_f32 v14, v168, v169
	v_cvt_pk_bf16_f32 v15, v166, v167
	global_store_dwordx4 v[16:17], v[12:15], off
	v_pk_mul_f32 v[166:167], v[32:33], s[8:9] op_sel_hi:[1,0]
	v_pk_mul_f32 v[168:169], v[30:31], s[8:9] op_sel_hi:[1,0]
	v_pk_mul_f32 v[14:15], v[40:41], s[8:9] op_sel_hi:[1,0]
	v_pk_mul_f32 v[12:13], v[38:39], s[8:9] op_sel_hi:[1,0]
	v_mad_i64_i32 v[6:7], s[24:25], v3, s50, v[6:7]
	v_cvt_pk_bf16_f32 v12, v12, v13
	v_cvt_pk_bf16_f32 v13, v14, v15
	v_cvt_pk_bf16_f32 v14, v168, v169
	v_cvt_pk_bf16_f32 v15, v166, v167
	global_store_dwordx4 v[16:17], v[12:15], off offset:256
	v_lshl_add_u64 v[6:7], v[6:7], 0, s[22:23]
	v_pk_mul_f32 v[16:17], v[28:29], s[8:9] op_sel_hi:[1,0]
	v_pk_mul_f32 v[14:15], v[36:37], s[8:9] op_sel_hi:[1,0]
	v_pk_mul_f32 v[12:13], v[34:35], s[8:9] op_sel_hi:[1,0]
	v_pk_mul_f32 v[166:167], v[26:27], s[8:9] op_sel_hi:[1,0]
	v_lshl_add_u64 v[6:7], v[6:7], 0, v[154:155]
	v_cvt_pk_bf16_f32 v12, v12, v13
	v_cvt_pk_bf16_f32 v13, v14, v15
	v_cvt_pk_bf16_f32 v14, v166, v167
	v_cvt_pk_bf16_f32 v15, v16, v17
	global_store_dwordx4 v[6:7], v[12:15], off
	v_pk_mul_f32 v[16:17], v[20:21], s[8:9] op_sel_hi:[1,0]
	v_pk_mul_f32 v[166:167], v[18:19], s[8:9] op_sel_hi:[1,0]
	v_pk_mul_f32 v[14:15], v[24:25], s[8:9] op_sel_hi:[1,0]
	v_pk_mul_f32 v[12:13], v[22:23], s[8:9] op_sel_hi:[1,0]
	s_mov_b64 s[22:23], 0
	v_cvt_pk_bf16_f32 v12, v12, v13
	v_cvt_pk_bf16_f32 v13, v14, v15
	v_cvt_pk_bf16_f32 v14, v166, v167
	v_cvt_pk_bf16_f32 v15, v16, v17
	global_store_dwordx4 v[6:7], v[12:15], off offset:256

.LBB0_942:
	s_add_u32 s29, s22, s28
	s_addc_u32 s53, s23, 0
	s_add_u32 s34, s29, 0x100
	s_addc_u32 s35, s53, 0
	s_and_b64 s[30:31], s[26:27], exec
	s_cselect_b32 s35, s13, s35
	s_cselect_b32 s34, s51, s34
	s_add_u32 s28, s20, s28
	s_addc_u32 s30, s21, 0
	s_add_u32 s28, s28, 0x100
	s_addc_u32 s30, s30, 0
	s_and_b64 s[26:27], s[26:27], exec
	s_cselect_b32 s37, s11, s30
	s_cselect_b32 s36, s52, s28
	s_add_u32 s62, s29, 0x10080
	s_addc_u32 s63, s53, 0
	s_add_i32 s65, s47, s33
	s_add_i32 m0, s19, 0xc000
	s_add_i32 s64, s19, 0xe000
	s_add_i32 s66, s65, 0x2000
	s_add_u32 s30, s36, 0x10000
	s_addc_u32 s31, s37, 0
	s_add_i32 s61, s48, s33
	ds_read_b128 v[2:5], v172
	ds_read_b128 v[6:9], v172 offset:1024
	ds_read_b128 v[10:13], v172 offset:2048
	ds_read_b128 v[14:17], v172 offset:3072
	s_add_i32 s60, s61, 0x2000
	s_add_i32 s59, 0, 0x18000
	s_add_u32 s28, s34, 0x10000
	s_addc_u32 s29, s35, 0
	s_add_i32 s57, s59, s33
	s_add_i32 s56, 0, 0x1c000
	s_add_i32 s55, s57, 0x2000
	s_add_u32 s26, s36, 0x10080
	s_addc_u32 s27, s37, 0
	s_add_i32 s54, s56, s33
	s_add_i32 s53, s54, 0x2000
	v_lshl_add_u64 v[158:159], s[62:63], 0, v[146:147]
	ds_read_b128 v[176:179], v173
	ds_read_b128 v[180:183], v173 offset:1024
	ds_read_b128 v[190:193], v173 offset:2048
	ds_read_b128 v[194:197], v173 offset:3072
	ds_read_b128 v[214:217], v173 offset:4096
	ds_read_b128 v[218:221], v173 offset:5120
	ds_read_b128 v[222:225], v173 offset:6144
	ds_read_b128 v[226:229], v173 offset:7168
	global_load_lds_dwordx4 v[158:159], off
	v_lshl_add_u64 v[158:159], s[62:63], 0, v[150:151]
	s_mov_b32 m0, s64
	s_nop 0
	global_load_lds_dwordx4 v[158:159], off
	s_waitcnt lgkmcnt(8)
	s_barrier
	s_waitcnt lgkmcnt(0)
	s_setprio 1
	s_waitcnt lgkmcnt(0)
	v_mfma_f32_16x16x128_f8f6f4 v[142:145], v[2:9], v[176:183], v[142:145]
	v_mfma_f32_16x16x128_f8f6f4 v[138:141], v[10:17], v[176:183], v[138:141]
	v_mfma_f32_16x16x128_f8f6f4 v[134:137], v[2:9], v[190:197], v[134:137]
	v_mfma_f32_16x16x128_f8f6f4 v[126:129], v[10:17], v[190:197], v[126:129]
	v_mfma_f32_16x16x128_f8f6f4 v[118:121], v[2:9], v[214:221], v[118:121]
	v_mfma_f32_16x16x128_f8f6f4 v[110:113], v[10:17], v[214:221], v[110:113]
	v_mfma_f32_16x16x128_f8f6f4 v[102:105], v[2:9], v[222:229], v[102:105]
	v_mfma_f32_16x16x128_f8f6f4 v[94:97], v[10:17], v[222:229], v[94:97]
	s_setprio 0
	s_barrier
	s_mov_b32 m0, s65
	v_lshl_add_u64 v[158:159], s[36:37], 0, v[148:149]
	ds_read_b128 v[230:233], v175
	ds_read_b128 v[234:237], v175 offset:1024
	ds_read_b128 v[238:241], v175 offset:2048
	ds_read_b128 v[242:245], v175 offset:3072
	global_load_lds_dwordx4 v[158:159], off
	v_lshl_add_u64 v[160:161], s[36:37], 0, v[152:153]
	s_mov_b32 m0, s66
	s_nop 0
	global_load_lds_dwordx4 v[160:161], off
	s_barrier
	s_waitcnt lgkmcnt(0)
	s_setprio 1
	s_waitcnt lgkmcnt(0)
	v_mfma_f32_16x16x128_f8f6f4 v[130:133], v[230:237], v[176:183], v[130:133]
	v_mfma_f32_16x16x128_f8f6f4 v[122:125], v[238:245], v[176:183], v[122:125]
	v_mfma_f32_16x16x128_f8f6f4 v[114:117], v[230:237], v[190:197], v[114:117]
	v_mfma_f32_16x16x128_f8f6f4 v[106:109], v[238:245], v[190:197], v[106:109]
	v_mfma_f32_16x16x128_f8f6f4 v[98:101], v[230:237], v[214:221], v[98:101]
	v_mfma_f32_16x16x128_f8f6f4 v[90:93], v[238:245], v[214:221], v[90:93]
	v_mfma_f32_16x16x128_f8f6f4 v[86:89], v[230:237], v[222:229], v[86:89]
	v_mfma_f32_16x16x128_f8f6f4 v[82:85], v[238:245], v[222:229], v[82:85]
	s_setprio 0
	s_mov_b32 m0, s19
	v_lshl_add_u64 v[162:163], s[34:35], 0, v[146:147]
	s_barrier
	ds_read_b128 v[176:179], v173 offset:16384
	ds_read_b128 v[180:183], v173 offset:17408
	ds_read_b128 v[190:193], v173 offset:18432
	ds_read_b128 v[194:197], v173 offset:19456
	ds_read_b128 v[214:217], v173 offset:20480
	ds_read_b128 v[218:221], v173 offset:21504
	ds_read_b128 v[222:225], v173 offset:22528
	ds_read_b128 v[226:229], v173 offset:23552
	global_load_lds_dwordx4 v[162:163], off
	v_lshl_add_u64 v[164:165], s[34:35], 0, v[150:151]
	s_mov_b32 m0, s39
	s_nop 0
	global_load_lds_dwordx4 v[164:165], off
	s_barrier
	s_waitcnt lgkmcnt(0)
	s_setprio 1
	s_waitcnt lgkmcnt(0)
	v_mfma_f32_16x16x128_f8f6f4 v[78:81], v[2:9], v[176:183], v[78:81]
	v_mfma_f32_16x16x128_f8f6f4 v[74:77], v[10:17], v[176:183], v[74:77]
	v_mfma_f32_16x16x128_f8f6f4 v[70:73], v[2:9], v[190:197], v[70:73]
	v_mfma_f32_16x16x128_f8f6f4 v[62:65], v[10:17], v[190:197], v[62:65]
	v_mfma_f32_16x16x128_f8f6f4 v[54:57], v[2:9], v[214:221], v[54:57]
	v_mfma_f32_16x16x128_f8f6f4 v[46:49], v[10:17], v[214:221], v[46:49]
	v_mfma_f32_16x16x128_f8f6f4 v[38:41], v[2:9], v[222:229], v[38:41]
	v_mfma_f32_16x16x128_f8f6f4 v[30:33], v[10:17], v[222:229], v[30:33]
	s_setprio 0
	s_barrier
	s_mov_b32 m0, s61
	v_lshl_add_u64 v[2:3], s[30:31], 0, v[148:149]
	global_load_lds_dwordx4 v[2:3], off
	v_lshl_add_u64 v[2:3], s[30:31], 0, v[152:153]
	s_mov_b32 m0, s60
	s_nop 0
	global_load_lds_dwordx4 v[2:3], off
	s_waitcnt vmcnt(6)
	s_barrier
	s_setprio 1
	v_mfma_f32_16x16x128_f8f6f4 v[66:69], v[230:237], v[176:183], v[66:69]
	v_mfma_f32_16x16x128_f8f6f4 v[58:61], v[238:245], v[176:183], v[58:61]
	v_mfma_f32_16x16x128_f8f6f4 v[50:53], v[230:237], v[190:197], v[50:53]
	v_mfma_f32_16x16x128_f8f6f4 v[42:45], v[238:245], v[190:197], v[42:45]
	v_mfma_f32_16x16x128_f8f6f4 v[34:37], v[230:237], v[214:221], v[34:37]
	v_mfma_f32_16x16x128_f8f6f4 v[26:29], v[238:245], v[214:221], v[26:29]
	v_mfma_f32_16x16x128_f8f6f4 v[22:25], v[230:237], v[222:229], v[22:25]
	v_mfma_f32_16x16x128_f8f6f4 v[18:21], v[238:245], v[222:229], v[18:21]
	s_setprio 0
	v_add_u32_e32 v14, s59, v170
	s_barrier
	ds_read_b128 v[2:5], v14
	ds_read_b128 v[6:9], v14 offset:1024
	ds_read_b128 v[10:13], v14 offset:2048
	ds_read_b128 v[14:17], v14 offset:3072
	s_mov_b32 m0, s40
	v_lshl_add_u64 v[184:185], s[28:29], 0, v[146:147]
	ds_read_b128 v[176:179], v173 offset:32768
	ds_read_b128 v[180:183], v173 offset:33792
	ds_read_b128 v[190:193], v173 offset:34816
	ds_read_b128 v[194:197], v173 offset:35840
	ds_read_b128 v[214:217], v173 offset:36864
	ds_read_b128 v[218:221], v173 offset:37888
	ds_read_b128 v[222:225], v173 offset:38912
	ds_read_b128 v[226:229], v173 offset:39936
	global_load_lds_dwordx4 v[184:185], off
	v_lshl_add_u64 v[184:185], s[28:29], 0, v[150:151]
	s_mov_b32 m0, s41
	s_nop 0
	global_load_lds_dwordx4 v[184:185], off
	s_waitcnt lgkmcnt(8)
	s_barrier
	s_waitcnt lgkmcnt(0)
	s_setprio 1
	s_waitcnt lgkmcnt(0)
	v_mfma_f32_16x16x128_f8f6f4 v[142:145], v[2:9], v[176:183], v[142:145]
	v_mfma_f32_16x16x128_f8f6f4 v[138:141], v[10:17], v[176:183], v[138:141]
	v_mfma_f32_16x16x128_f8f6f4 v[134:137], v[2:9], v[190:197], v[134:137]
	v_mfma_f32_16x16x128_f8f6f4 v[126:129], v[10:17], v[190:197], v[126:129]
	v_mfma_f32_16x16x128_f8f6f4 v[118:121], v[2:9], v[214:221], v[118:121]
	v_mfma_f32_16x16x128_f8f6f4 v[110:113], v[10:17], v[214:221], v[110:113]
	v_mfma_f32_16x16x128_f8f6f4 v[102:105], v[2:9], v[222:229], v[102:105]
	v_mfma_f32_16x16x128_f8f6f4 v[94:97], v[10:17], v[222:229], v[94:97]
	s_setprio 0
	s_barrier
	s_mov_b32 m0, s57
	v_add_u32_e32 v184, s56, v170
	v_lshl_add_u64 v[158:159], v[158:159], 0, s[6:7]
	ds_read_b128 v[230:233], v184
	ds_read_b128 v[234:237], v184 offset:1024
	ds_read_b128 v[238:241], v184 offset:2048
	ds_read_b128 v[242:245], v184 offset:3072
	global_load_lds_dwordx4 v[158:159], off
	v_lshl_add_u64 v[158:159], v[160:161], 0, s[6:7]
	s_mov_b32 m0, s55
	s_nop 0
	global_load_lds_dwordx4 v[158:159], off
	s_barrier
	s_waitcnt lgkmcnt(0)
	s_setprio 1
	s_waitcnt lgkmcnt(0)
	v_mfma_f32_16x16x128_f8f6f4 v[130:133], v[230:237], v[176:183], v[130:133]
	v_mfma_f32_16x16x128_f8f6f4 v[122:125], v[238:245], v[176:183], v[122:125]
	v_mfma_f32_16x16x128_f8f6f4 v[114:117], v[230:237], v[190:197], v[114:117]
	v_mfma_f32_16x16x128_f8f6f4 v[106:109], v[238:245], v[190:197], v[106:109]
	v_mfma_f32_16x16x128_f8f6f4 v[98:101], v[230:237], v[214:221], v[98:101]
	v_mfma_f32_16x16x128_f8f6f4 v[90:93], v[238:245], v[214:221], v[90:93]
	v_mfma_f32_16x16x128_f8f6f4 v[86:89], v[230:237], v[222:229], v[86:89]
	v_mfma_f32_16x16x128_f8f6f4 v[82:85], v[238:245], v[222:229], v[82:85]
	s_setprio 0
	s_mov_b32 m0, s43
	v_lshl_add_u64 v[158:159], v[162:163], 0, s[6:7]
	s_barrier
	ds_read_b128 v[176:179], v173 offset:49152
	ds_read_b128 v[180:183], v173 offset:50176
	ds_read_b128 v[190:193], v173 offset:51200
	ds_read_b128 v[194:197], v173 offset:52224
	ds_read_b128 v[214:217], v173 offset:53248
	ds_read_b128 v[218:221], v173 offset:54272
	ds_read_b128 v[222:225], v173 offset:55296
	ds_read_b128 v[226:229], v173 offset:56320
	global_load_lds_dwordx4 v[158:159], off
	v_lshl_add_u64 v[158:159], v[164:165], 0, s[6:7]
	s_mov_b32 m0, s44
	s_nop 0
	global_load_lds_dwordx4 v[158:159], off
	s_barrier
	s_waitcnt lgkmcnt(0)
	s_setprio 1
	s_waitcnt lgkmcnt(0)
	v_mfma_f32_16x16x128_f8f6f4 v[78:81], v[2:9], v[176:183], v[78:81]
	v_mfma_f32_16x16x128_f8f6f4 v[74:77], v[10:17], v[176:183], v[74:77]
	v_mfma_f32_16x16x128_f8f6f4 v[70:73], v[2:9], v[190:197], v[70:73]
	v_mfma_f32_16x16x128_f8f6f4 v[62:65], v[10:17], v[190:197], v[62:65]
	v_mfma_f32_16x16x128_f8f6f4 v[54:57], v[2:9], v[214:221], v[54:57]
	v_mfma_f32_16x16x128_f8f6f4 v[46:49], v[10:17], v[214:221], v[46:49]
	v_mfma_f32_16x16x128_f8f6f4 v[38:41], v[2:9], v[222:229], v[38:41]
	v_mfma_f32_16x16x128_f8f6f4 v[30:33], v[10:17], v[222:229], v[30:33]
	s_setprio 0
	s_barrier
	s_mov_b32 m0, s54
	v_lshl_add_u64 v[2:3], s[26:27], 0, v[148:149]
	global_load_lds_dwordx4 v[2:3], off
	v_lshl_add_u64 v[2:3], s[26:27], 0, v[152:153]
	s_mov_b32 m0, s53
	s_nop 0
	global_load_lds_dwordx4 v[2:3], off
	s_waitcnt vmcnt(6)
	s_barrier
	s_setprio 1
	v_mfma_f32_16x16x128_f8f6f4 v[66:69], v[230:237], v[176:183], v[66:69]
	v_mfma_f32_16x16x128_f8f6f4 v[58:61], v[238:245], v[176:183], v[58:61]
	v_mfma_f32_16x16x128_f8f6f4 v[50:53], v[230:237], v[190:197], v[50:53]
	v_mfma_f32_16x16x128_f8f6f4 v[42:45], v[238:245], v[190:197], v[42:45]
	v_mfma_f32_16x16x128_f8f6f4 v[34:37], v[230:237], v[214:221], v[34:37]
	v_mfma_f32_16x16x128_f8f6f4 v[26:29], v[238:245], v[214:221], v[26:29]
	v_mfma_f32_16x16x128_f8f6f4 v[22:25], v[230:237], v[222:229], v[22:25]
	v_mfma_f32_16x16x128_f8f6f4 v[18:21], v[238:245], v[222:229], v[18:21]
	s_setprio 0
	s_movk_i32 s28, 0x100
	s_andn2_b64 vcc, exec, s[24:25]
	s_mov_b64 s[26:27], -1
	s_mov_b64 s[24:25], 0
	s_barrier
	s_cbranch_vccz .LBB0_942
	v_lshl_or_b32 v4, s50, 8, v171
	v_lshl_add_u32 v16, s18, 8, v169
	v_ashrrev_i32_e32 v5, 31, v4
	v_mov_b64_e32 v[2:3], s[4:5]
	v_mad_i64_i32 v[6:7], s[20:21], v16, s49, v[2:3]
	v_lshlrev_b64 v[4:5], 1, v[4:5]
	v_lshl_add_u64 v[10:11], v[6:7], 0, v[4:5]
	v_pk_mul_f32 v[8:9], v[144:145], s[8:9] op_sel_hi:[1,0]
	v_pk_mul_f32 v[6:7], v[142:143], s[8:9] op_sel_hi:[1,0]
	v_pk_mul_f32 v[12:13], v[140:141], s[8:9] op_sel_hi:[1,0]
	v_pk_mul_f32 v[14:15], v[138:139], s[8:9] op_sel_hi:[1,0]
	v_cvt_pk_bf16_f32 v6, v6, v7
	v_cvt_pk_bf16_f32 v7, v8, v9
	v_cvt_pk_bf16_f32 v8, v14, v15
	v_cvt_pk_bf16_f32 v9, v12, v13
	global_store_dwordx4 v[10:11], v[6:9], off
	v_pk_mul_f32 v[12:13], v[124:125], s[8:9] op_sel_hi:[1,0]
	v_pk_mul_f32 v[14:15], v[122:123], s[8:9] op_sel_hi:[1,0]
	v_pk_mul_f32 v[8:9], v[132:133], s[8:9] op_sel_hi:[1,0]
	v_pk_mul_f32 v[6:7], v[130:131], s[8:9] op_sel_hi:[1,0]
	s_and_b64 vcc, exec, s[0:1]
	v_cvt_pk_bf16_f32 v6, v6, v7
	v_cvt_pk_bf16_f32 v7, v8, v9
	v_cvt_pk_bf16_f32 v8, v14, v15
	v_cvt_pk_bf16_f32 v9, v12, v13
	global_store_dwordx4 v[10:11], v[6:9], off offset:256
	v_pk_mul_f32 v[12:13], v[128:129], s[8:9] op_sel_hi:[1,0]
	v_pk_mul_f32 v[14:15], v[126:127], s[8:9] op_sel_hi:[1,0]
	v_or_b32_e32 v6, 16, v16
	v_mad_i64_i32 v[6:7], s[20:21], v6, s49, v[2:3]
	v_lshl_add_u64 v[10:11], v[6:7], 0, v[4:5]
	v_pk_mul_f32 v[8:9], v[136:137], s[8:9] op_sel_hi:[1,0]
	v_pk_mul_f32 v[6:7], v[134:135], s[8:9] op_sel_hi:[1,0]
	s_mov_b32 s50, s10
	v_cvt_pk_bf16_f32 v6, v6, v7
	v_cvt_pk_bf16_f32 v7, v8, v9
	v_cvt_pk_bf16_f32 v8, v14, v15
	v_cvt_pk_bf16_f32 v9, v12, v13
	global_store_dwordx4 v[10:11], v[6:9], off
	v_pk_mul_f32 v[12:13], v[108:109], s[8:9] op_sel_hi:[1,0]
	v_pk_mul_f32 v[14:15], v[106:107], s[8:9] op_sel_hi:[1,0]
	v_pk_mul_f32 v[8:9], v[116:117], s[8:9] op_sel_hi:[1,0]
	v_pk_mul_f32 v[6:7], v[114:115], s[8:9] op_sel_hi:[1,0]
	s_mov_b32 s18, s12
	v_cvt_pk_bf16_f32 v6, v6, v7
	v_cvt_pk_bf16_f32 v7, v8, v9
	v_cvt_pk_bf16_f32 v8, v14, v15
	v_cvt_pk_bf16_f32 v9, v12, v13
	global_store_dwordx4 v[10:11], v[6:9], off offset:256
	v_pk_mul_f32 v[12:13], v[112:113], s[8:9] op_sel_hi:[1,0]
	v_pk_mul_f32 v[14:15], v[110:111], s[8:9] op_sel_hi:[1,0]
	v_or_b32_e32 v6, 32, v16
	v_mad_i64_i32 v[6:7], s[20:21], v6, s49, v[2:3]
	v_lshl_add_u64 v[10:11], v[6:7], 0, v[4:5]
	v_pk_mul_f32 v[8:9], v[120:121], s[8:9] op_sel_hi:[1,0]
	v_pk_mul_f32 v[6:7], v[118:119], s[8:9] op_sel_hi:[1,0]
	s_mov_b64 s[22:23], s[14:15]
	v_cvt_pk_bf16_f32 v6, v6, v7
	v_cvt_pk_bf16_f32 v7, v8, v9
	v_cvt_pk_bf16_f32 v8, v14, v15
	v_cvt_pk_bf16_f32 v9, v12, v13
	global_store_dwordx4 v[10:11], v[6:9], off
	v_pk_mul_f32 v[12:13], v[92:93], s[8:9] op_sel_hi:[1,0]
	v_pk_mul_f32 v[14:15], v[90:91], s[8:9] op_sel_hi:[1,0]
	v_pk_mul_f32 v[8:9], v[100:101], s[8:9] op_sel_hi:[1,0]
	v_pk_mul_f32 v[6:7], v[98:99], s[8:9] op_sel_hi:[1,0]
	s_nop 0
	v_cvt_pk_bf16_f32 v6, v6, v7
	v_cvt_pk_bf16_f32 v7, v8, v9
	v_cvt_pk_bf16_f32 v8, v14, v15
	v_cvt_pk_bf16_f32 v9, v12, v13
	global_store_dwordx4 v[10:11], v[6:9], off offset:256
	v_pk_mul_f32 v[12:13], v[96:97], s[8:9] op_sel_hi:[1,0]
	v_pk_mul_f32 v[14:15], v[94:95], s[8:9] op_sel_hi:[1,0]
	v_or_b32_e32 v6, 48, v16
	v_mad_i64_i32 v[6:7], s[20:21], v6, s49, v[2:3]
	v_lshl_add_u64 v[10:11], v[6:7], 0, v[4:5]
	v_pk_mul_f32 v[8:9], v[104:105], s[8:9] op_sel_hi:[1,0]
	v_pk_mul_f32 v[6:7], v[102:103], s[8:9] op_sel_hi:[1,0]
	s_nop 0
	v_cvt_pk_bf16_f32 v6, v6, v7
	v_cvt_pk_bf16_f32 v7, v8, v9
	v_cvt_pk_bf16_f32 v8, v14, v15
	v_cvt_pk_bf16_f32 v9, v12, v13
	global_store_dwordx4 v[10:11], v[6:9], off
	v_pk_mul_f32 v[12:13], v[84:85], s[8:9] op_sel_hi:[1,0]
	v_pk_mul_f32 v[14:15], v[82:83], s[8:9] op_sel_hi:[1,0]
	v_pk_mul_f32 v[8:9], v[88:89], s[8:9] op_sel_hi:[1,0]
	v_pk_mul_f32 v[6:7], v[86:87], s[8:9] op_sel_hi:[1,0]
	s_nop 0
	v_cvt_pk_bf16_f32 v6, v6, v7
	v_cvt_pk_bf16_f32 v7, v8, v9
	v_cvt_pk_bf16_f32 v8, v14, v15
	v_cvt_pk_bf16_f32 v9, v12, v13
	global_store_dwordx4 v[10:11], v[6:9], off offset:256
	v_pk_mul_f32 v[12:13], v[76:77], s[8:9] op_sel_hi:[1,0]
	v_pk_mul_f32 v[14:15], v[74:75], s[8:9] op_sel_hi:[1,0]
	v_add_u32_e32 v6, 0x80, v16
	v_mad_i64_i32 v[6:7], s[20:21], v6, s49, v[2:3]
	v_lshl_add_u64 v[10:11], v[6:7], 0, v[4:5]
	v_pk_mul_f32 v[8:9], v[80:81], s[8:9] op_sel_hi:[1,0]
	v_pk_mul_f32 v[6:7], v[78:79], s[8:9] op_sel_hi:[1,0]
	s_nop 0
	v_cvt_pk_bf16_f32 v6, v6, v7
	v_cvt_pk_bf16_f32 v7, v8, v9
	v_cvt_pk_bf16_f32 v8, v14, v15
	v_cvt_pk_bf16_f32 v9, v12, v13
	global_store_dwordx4 v[10:11], v[6:9], off
	v_pk_mul_f32 v[12:13], v[60:61], s[8:9] op_sel_hi:[1,0]
	v_pk_mul_f32 v[14:15], v[58:59], s[8:9] op_sel_hi:[1,0]
	v_pk_mul_f32 v[8:9], v[68:69], s[8:9] op_sel_hi:[1,0]
	v_pk_mul_f32 v[6:7], v[66:67], s[8:9] op_sel_hi:[1,0]
	s_nop 0
	v_cvt_pk_bf16_f32 v6, v6, v7
	v_cvt_pk_bf16_f32 v7, v8, v9
	v_cvt_pk_bf16_f32 v8, v14, v15
	v_cvt_pk_bf16_f32 v9, v12, v13
	global_store_dwordx4 v[10:11], v[6:9], off offset:256
	v_pk_mul_f32 v[12:13], v[64:65], s[8:9] op_sel_hi:[1,0]
	v_pk_mul_f32 v[14:15], v[62:63], s[8:9] op_sel_hi:[1,0]
	v_add_u32_e32 v6, 0x90, v16
	v_mad_i64_i32 v[6:7], s[20:21], v6, s49, v[2:3]
	v_lshl_add_u64 v[10:11], v[6:7], 0, v[4:5]
	v_pk_mul_f32 v[8:9], v[72:73], s[8:9] op_sel_hi:[1,0]
	v_pk_mul_f32 v[6:7], v[70:71], s[8:9] op_sel_hi:[1,0]
	s_nop 0
	v_cvt_pk_bf16_f32 v6, v6, v7
	v_cvt_pk_bf16_f32 v7, v8, v9
	v_cvt_pk_bf16_f32 v8, v14, v15
	v_cvt_pk_bf16_f32 v9, v12, v13
	global_store_dwordx4 v[10:11], v[6:9], off
	v_pk_mul_f32 v[12:13], v[44:45], s[8:9] op_sel_hi:[1,0]
	v_pk_mul_f32 v[14:15], v[42:43], s[8:9] op_sel_hi:[1,0]
	v_pk_mul_f32 v[8:9], v[52:53], s[8:9] op_sel_hi:[1,0]
	v_pk_mul_f32 v[6:7], v[50:51], s[8:9] op_sel_hi:[1,0]
	s_nop 0
	v_cvt_pk_bf16_f32 v6, v6, v7
	v_cvt_pk_bf16_f32 v7, v8, v9
	v_cvt_pk_bf16_f32 v8, v14, v15
	v_cvt_pk_bf16_f32 v9, v12, v13
	global_store_dwordx4 v[10:11], v[6:9], off offset:256
	v_pk_mul_f32 v[12:13], v[48:49], s[8:9] op_sel_hi:[1,0]
	v_pk_mul_f32 v[14:15], v[46:47], s[8:9] op_sel_hi:[1,0]
	v_add_u32_e32 v6, 0xa0, v16
	v_mad_i64_i32 v[6:7], s[20:21], v6, s49, v[2:3]
	v_lshl_add_u64 v[10:11], v[6:7], 0, v[4:5]
	v_pk_mul_f32 v[8:9], v[56:57], s[8:9] op_sel_hi:[1,0]
	v_pk_mul_f32 v[6:7], v[54:55], s[8:9] op_sel_hi:[1,0]
	s_nop 0
	v_cvt_pk_bf16_f32 v6, v6, v7
	v_cvt_pk_bf16_f32 v7, v8, v9
	v_cvt_pk_bf16_f32 v8, v14, v15
	v_cvt_pk_bf16_f32 v9, v12, v13
	global_store_dwordx4 v[10:11], v[6:9], off
	v_pk_mul_f32 v[12:13], v[28:29], s[8:9] op_sel_hi:[1,0]
	v_pk_mul_f32 v[14:15], v[26:27], s[8:9] op_sel_hi:[1,0]
	v_pk_mul_f32 v[8:9], v[36:37], s[8:9] op_sel_hi:[1,0]
	v_pk_mul_f32 v[6:7], v[34:35], s[8:9] op_sel_hi:[1,0]
	s_nop 0
	v_cvt_pk_bf16_f32 v6, v6, v7
	v_cvt_pk_bf16_f32 v7, v8, v9
	v_cvt_pk_bf16_f32 v8, v14, v15
	v_cvt_pk_bf16_f32 v9, v12, v13
	global_store_dwordx4 v[10:11], v[6:9], off offset:256
	v_pk_mul_f32 v[10:11], v[30:31], s[8:9] op_sel_hi:[1,0]
	s_nop 0
	v_add_u32_e32 v6, 0xb0, v16
	v_mad_i64_i32 v[2:3], s[20:21], v6, s49, v[2:3]
	v_lshl_add_u64 v[6:7], v[2:3], 0, v[4:5]
	v_pk_mul_f32 v[4:5], v[40:41], s[8:9] op_sel_hi:[1,0]
	v_pk_mul_f32 v[2:3], v[38:39], s[8:9] op_sel_hi:[1,0]
	v_pk_mul_f32 v[8:9], v[32:33], s[8:9] op_sel_hi:[1,0]
	v_cvt_pk_bf16_f32 v2, v2, v3
	v_cvt_pk_bf16_f32 v3, v4, v5
	v_cvt_pk_bf16_f32 v4, v10, v11
	v_cvt_pk_bf16_f32 v5, v8, v9
	global_store_dwordx4 v[6:7], v[2:5], off
	v_pk_mul_f32 v[8:9], v[20:21], s[8:9] op_sel_hi:[1,0]
	v_pk_mul_f32 v[10:11], v[18:19], s[8:9] op_sel_hi:[1,0]
	v_pk_mul_f32 v[4:5], v[24:25], s[8:9] op_sel_hi:[1,0]
	v_pk_mul_f32 v[2:3], v[22:23], s[8:9] op_sel_hi:[1,0]
	s_mov_b64 s[20:21], s[16:17]
	v_cvt_pk_bf16_f32 v2, v2, v3
	v_cvt_pk_bf16_f32 v3, v4, v5
	v_cvt_pk_bf16_f32 v4, v10, v11
	v_cvt_pk_bf16_f32 v5, v8, v9
	global_store_dwordx4 v[6:7], v[2:5], off offset:256
	s_cbranch_vccz .LBB0_939
	s_waitcnt vmcnt(0)
	s_cmpk_gt_u32 s2, 0xff
	s_cbranch_scc1 .LBB0_946
	s_barrier

.LBB0_951:
	s_ashr_i32 s31, s30, 31
	s_lshl_b64 s[34:35], s[30:31], 17
	s_add_u32 s34, s3, s34
	s_addc_u32 s35, s17, s35
	ds_read_b128 v[14:17], v158
	ds_read_b128 v[18:21], v158 offset:1024
	ds_read_b128 v[30:33], v158 offset:2048
	ds_read_b128 v[34:37], v158 offset:3072
	s_and_b64 s[36:37], s[4:5], exec
	s_cselect_b32 s41, s35, s43
	s_cselect_b32 s40, s34, s42
	s_ashr_i32 s29, s28, 31
	s_lshl_b64 s[36:37], s[28:29], 17
	s_add_u32 s36, s19, s36
	s_addc_u32 s37, s33, s37
	s_and_b64 s[4:5], s[4:5], exec
	s_cselect_b32 s5, s37, s45
	s_cselect_b32 s4, s36, s44
	s_add_u32 s60, s42, 0x10080
	s_addc_u32 s61, s43, 0
	s_add_i32 s65, s39, 0xc000
	v_lshl_add_u64 v[54:55], s[60:61], 0, v[146:147]
	s_mov_b32 m0, s65
	s_add_i32 s29, s39, 0xe000
	ds_read_b128 v[6:9], v159
	ds_read_b128 v[10:13], v159 offset:1024
	ds_read_b128 v[22:25], v159 offset:2048
	ds_read_b128 v[26:29], v159 offset:3072
	ds_read_b128 v[38:41], v159 offset:4096
	ds_read_b128 v[42:45], v159 offset:5120
	ds_read_b128 v[46:49], v159 offset:6144
	ds_read_b128 v[50:53], v159 offset:7168
	global_load_lds_dwordx4 v[54:55], off
	v_lshl_add_u64 v[54:55], s[60:61], 0, v[150:151]
	s_mov_b32 m0, s29
	s_nop 0
	global_load_lds_dwordx4 v[54:55], off
	s_waitcnt lgkmcnt(8)
	s_barrier
	s_waitcnt lgkmcnt(0)
	s_setprio 1
	v_mov_b64_e32 v[124:125], v[4:5]
	v_mov_b64_e32 v[120:121], v[4:5]
	v_mov_b64_e32 v[108:109], v[4:5]
	v_mov_b64_e32 v[104:105], v[4:5]
	v_mov_b64_e32 v[92:93], v[4:5]
	v_mov_b64_e32 v[88:89], v[4:5]
	v_mov_b64_e32 v[60:61], v[4:5]
	v_mov_b64_e32 v[56:57], v[4:5]
	v_mov_b64_e32 v[122:123], v[2:3]
	v_mov_b64_e32 v[118:119], v[2:3]
	v_mov_b64_e32 v[106:107], v[2:3]
	v_mov_b64_e32 v[102:103], v[2:3]
	v_mov_b64_e32 v[90:91], v[2:3]
	v_mov_b64_e32 v[86:87], v[2:3]
	v_mov_b64_e32 v[58:59], v[2:3]
	v_mov_b64_e32 v[54:55], v[2:3]
	s_waitcnt lgkmcnt(0)
	v_mfma_f32_16x16x128_f8f6f4 v[122:125], v[14:21], v[6:13], v[122:125]
	v_mfma_f32_16x16x128_f8f6f4 v[118:121], v[30:37], v[6:13], v[118:121]
	v_mfma_f32_16x16x128_f8f6f4 v[106:109], v[14:21], v[22:29], v[106:109]
	v_mfma_f32_16x16x128_f8f6f4 v[102:105], v[30:37], v[22:29], v[102:105]
	v_mfma_f32_16x16x128_f8f6f4 v[90:93], v[14:21], v[38:45], v[90:93]
	v_mfma_f32_16x16x128_f8f6f4 v[86:89], v[30:37], v[38:45], v[86:89]
	v_mfma_f32_16x16x128_f8f6f4 v[58:61], v[14:21], v[46:53], v[58:61]
	v_mfma_f32_16x16x128_f8f6f4 v[54:57], v[30:37], v[46:53], v[54:57]
	s_setprio 0
	s_barrier
	v_lshl_add_u64 v[140:141], s[44:45], 0, v[148:149]
	s_add_i32 s63, s55, s46
	v_lshl_add_u64 v[62:63], v[140:141], 0, s[6:7]
	s_mov_b32 m0, s63
	v_lshl_add_u64 v[142:143], s[44:45], 0, v[152:153]
	s_add_i32 s31, s63, 0x2000
	ds_read_b128 v[164:167], v161
	ds_read_b128 v[168:171], v161 offset:1024
	ds_read_b128 v[172:175], v161 offset:2048
	ds_read_b128 v[176:179], v161 offset:3072
	global_load_lds_dwordx4 v[62:63], off
	v_lshl_add_u64 v[62:63], v[142:143], 0, s[6:7]
	s_mov_b32 m0, s31
	s_nop 0
	global_load_lds_dwordx4 v[62:63], off
	s_barrier
	s_waitcnt lgkmcnt(0)
	s_setprio 1
	v_mov_b64_e32 v[132:133], v[4:5]
	v_mov_b64_e32 v[128:129], v[4:5]
	v_mov_b64_e32 v[116:117], v[4:5]
	v_mov_b64_e32 v[112:113], v[4:5]
	v_mov_b64_e32 v[100:101], v[4:5]
	v_mov_b64_e32 v[96:97], v[4:5]
	v_mov_b64_e32 v[68:69], v[4:5]
	v_mov_b64_e32 v[64:65], v[4:5]
	v_mov_b64_e32 v[130:131], v[2:3]
	v_mov_b64_e32 v[126:127], v[2:3]
	v_mov_b64_e32 v[114:115], v[2:3]
	v_mov_b64_e32 v[110:111], v[2:3]
	v_mov_b64_e32 v[98:99], v[2:3]
	v_mov_b64_e32 v[94:95], v[2:3]
	v_mov_b64_e32 v[66:67], v[2:3]
	v_mov_b64_e32 v[62:63], v[2:3]
	s_waitcnt lgkmcnt(0)
	v_mfma_f32_16x16x128_f8f6f4 v[130:133], v[164:171], v[6:13], v[130:133]
	v_mfma_f32_16x16x128_f8f6f4 v[126:129], v[172:179], v[6:13], v[126:129]
	v_mfma_f32_16x16x128_f8f6f4 v[114:117], v[164:171], v[22:29], v[114:117]
	v_mfma_f32_16x16x128_f8f6f4 v[110:113], v[172:179], v[22:29], v[110:113]
	v_mfma_f32_16x16x128_f8f6f4 v[98:101], v[164:171], v[38:45], v[98:101]
	v_mfma_f32_16x16x128_f8f6f4 v[94:97], v[172:179], v[38:45], v[94:97]
	v_mfma_f32_16x16x128_f8f6f4 v[66:69], v[164:171], v[46:53], v[66:69]
	v_mfma_f32_16x16x128_f8f6f4 v[62:65], v[172:179], v[46:53], v[62:65]
	s_setprio 0
	v_lshl_add_u64 v[144:145], s[42:43], 0, v[146:147]
	s_mov_b32 m0, s39
	v_lshl_add_u64 v[6:7], v[144:145], 0, s[6:7]
	v_lshl_add_u64 v[154:155], s[42:43], 0, v[150:151]
	s_barrier
	ds_read_b128 v[46:49], v159 offset:16384
	ds_read_b128 v[50:53], v159 offset:17408
	ds_read_b128 v[180:183], v159 offset:18432
	ds_read_b128 v[184:187], v159 offset:19456
	ds_read_b128 v[190:193], v159 offset:20480
	ds_read_b128 v[194:197], v159 offset:21504
	ds_read_b128 v[214:217], v159 offset:22528
	ds_read_b128 v[218:221], v159 offset:23552
	global_load_lds_dwordx4 v[6:7], off
	v_lshl_add_u64 v[6:7], v[154:155], 0, s[6:7]
	s_mov_b32 m0, s48
	s_nop 0
	global_load_lds_dwordx4 v[6:7], off
	s_barrier
	s_waitcnt lgkmcnt(0)
	s_setprio 1
	v_mov_b64_e32 v[76:77], v[4:5]
	v_mov_b64_e32 v[72:73], v[4:5]
	v_mov_b64_e32 v[44:45], v[4:5]
	v_mov_b64_e32 v[40:41], v[4:5]
	v_mov_b64_e32 v[28:29], v[4:5]
	v_mov_b64_e32 v[24:25], v[4:5]
	v_mov_b64_e32 v[12:13], v[4:5]
	v_mov_b64_e32 v[8:9], v[4:5]
	v_mov_b64_e32 v[74:75], v[2:3]
	v_mov_b64_e32 v[70:71], v[2:3]
	v_mov_b64_e32 v[42:43], v[2:3]
	v_mov_b64_e32 v[38:39], v[2:3]
	v_mov_b64_e32 v[26:27], v[2:3]
	v_mov_b64_e32 v[22:23], v[2:3]
	v_mov_b64_e32 v[10:11], v[2:3]
	v_mov_b64_e32 v[6:7], v[2:3]
	s_waitcnt lgkmcnt(0)
	v_mfma_f32_16x16x128_f8f6f4 v[74:77], v[14:21], v[46:53], v[74:77]
	v_mfma_f32_16x16x128_f8f6f4 v[70:73], v[30:37], v[46:53], v[70:73]
	v_mfma_f32_16x16x128_f8f6f4 v[42:45], v[14:21], v[180:187], v[42:45]
	v_mfma_f32_16x16x128_f8f6f4 v[38:41], v[30:37], v[180:187], v[38:41]
	v_mfma_f32_16x16x128_f8f6f4 v[26:29], v[14:21], v[190:197], v[26:29]
	v_mfma_f32_16x16x128_f8f6f4 v[22:25], v[30:37], v[190:197], v[22:25]
	v_mfma_f32_16x16x128_f8f6f4 v[10:13], v[14:21], v[214:221], v[10:13]
	v_mfma_f32_16x16x128_f8f6f4 v[6:9], v[30:37], v[214:221], v[6:9]
	s_setprio 0
	s_barrier
	s_add_u32 s66, s44, 0x10100
	s_addc_u32 s67, s45, 0
	s_add_i32 s61, s56, s46
	v_lshl_add_u64 v[14:15], s[66:67], 0, v[148:149]
	s_mov_b32 m0, s61
	s_add_i32 s60, s61, 0x2000
	global_load_lds_dwordx4 v[14:15], off
	v_lshl_add_u64 v[14:15], s[66:67], 0, v[152:153]
	s_mov_b32 m0, s60
	s_nop 0
	global_load_lds_dwordx4 v[14:15], off
	s_waitcnt vmcnt(6)
	s_barrier
	s_setprio 1
	v_mov_b64_e32 v[84:85], v[4:5]
	v_mov_b64_e32 v[80:81], v[4:5]
	v_mov_b64_e32 v[82:83], v[2:3]
	v_mov_b64_e32 v[78:79], v[2:3]
	v_mfma_f32_16x16x128_f8f6f4 v[82:85], v[164:171], v[46:53], v[82:85]
	v_mfma_f32_16x16x128_f8f6f4 v[78:81], v[172:179], v[46:53], v[78:81]
	v_mov_b64_e32 v[52:53], v[4:5]
	v_mov_b64_e32 v[48:49], v[4:5]
	v_mov_b64_e32 v[36:37], v[4:5]
	v_mov_b64_e32 v[32:33], v[4:5]
	v_mov_b64_e32 v[20:21], v[4:5]
	v_mov_b64_e32 v[16:17], v[4:5]
	v_mov_b64_e32 v[50:51], v[2:3]
	v_mov_b64_e32 v[46:47], v[2:3]
	v_mov_b64_e32 v[34:35], v[2:3]
	v_mov_b64_e32 v[30:31], v[2:3]
	v_mov_b64_e32 v[18:19], v[2:3]
	v_mov_b64_e32 v[14:15], v[2:3]
	v_mfma_f32_16x16x128_f8f6f4 v[50:53], v[164:171], v[180:187], v[50:53]
	v_mfma_f32_16x16x128_f8f6f4 v[46:49], v[172:179], v[180:187], v[46:49]
	v_mfma_f32_16x16x128_f8f6f4 v[34:37], v[164:171], v[190:197], v[34:37]
	v_mfma_f32_16x16x128_f8f6f4 v[30:33], v[172:179], v[190:197], v[30:33]
	v_mfma_f32_16x16x128_f8f6f4 v[18:21], v[164:171], v[214:221], v[18:21]
	v_mfma_f32_16x16x128_f8f6f4 v[14:17], v[172:179], v[214:221], v[14:17]
	s_setprio 0
	s_add_i32 s64, 0, 0x18000
	v_add_u32_e32 v163, s64, v157
	s_barrier
	ds_read_b128 v[166:169], v163
	ds_read_b128 v[170:173], v163 offset:1024
	ds_read_b128 v[174:177], v163 offset:2048
	ds_read_b128 v[178:181], v163 offset:3072
	s_add_u32 s66, s42, 0x10100
	s_addc_u32 s67, s43, 0
	s_mov_b32 m0, s49
	v_lshl_add_u64 v[164:165], s[66:67], 0, v[146:147]
	ds_read_b128 v[190:193], v159 offset:32768
	ds_read_b128 v[194:197], v159 offset:33792
	ds_read_b128 v[214:217], v159 offset:34816
	ds_read_b128 v[218:221], v159 offset:35840
	ds_read_b128 v[222:225], v159 offset:36864
	ds_read_b128 v[226:229], v159 offset:37888
	ds_read_b128 v[230:233], v159 offset:38912
	ds_read_b128 v[234:237], v159 offset:39936
	global_load_lds_dwordx4 v[164:165], off
	v_lshl_add_u64 v[164:165], s[66:67], 0, v[150:151]
	s_mov_b32 m0, s50
	s_nop 0
	global_load_lds_dwordx4 v[164:165], off
	s_waitcnt lgkmcnt(8)
	s_barrier
	s_waitcnt lgkmcnt(0)
	s_setprio 1
	s_waitcnt lgkmcnt(0)
	v_mfma_f32_16x16x128_f8f6f4 v[122:125], v[166:173], v[190:197], v[122:125]
	v_mfma_f32_16x16x128_f8f6f4 v[118:121], v[174:181], v[190:197], v[118:121]
	v_mfma_f32_16x16x128_f8f6f4 v[106:109], v[166:173], v[214:221], v[106:109]
	v_mfma_f32_16x16x128_f8f6f4 v[102:105], v[174:181], v[214:221], v[102:105]
	v_mfma_f32_16x16x128_f8f6f4 v[90:93], v[166:173], v[222:229], v[90:93]
	v_mfma_f32_16x16x128_f8f6f4 v[86:89], v[174:181], v[222:229], v[86:89]
	v_mfma_f32_16x16x128_f8f6f4 v[58:61], v[166:173], v[230:237], v[58:61]
	v_mfma_f32_16x16x128_f8f6f4 v[54:57], v[174:181], v[230:237], v[54:57]
	s_setprio 0
	s_barrier
	s_add_i32 s68, 0, 0x1c000
	s_add_i32 s64, s64, s46
	v_add_u32_e32 v164, s68, v157
	v_lshl_add_u64 v[140:141], v[140:141], 0, s[14:15]
	s_mov_b32 m0, s64
	s_add_i32 s62, s64, 0x2000
	ds_read_b128 v[238:241], v164
	ds_read_b128 v[242:245], v164 offset:1024
	ds_read_b128 v[246:249], v164 offset:2048
	ds_read_b128 v[250:253], v164 offset:3072
	global_load_lds_dwordx4 v[140:141], off
	v_lshl_add_u64 v[140:141], v[142:143], 0, s[14:15]
	s_mov_b32 m0, s62
	s_nop 0
	global_load_lds_dwordx4 v[140:141], off
	s_barrier
	s_waitcnt lgkmcnt(0)
	s_setprio 1
	s_waitcnt lgkmcnt(0)
	v_mfma_f32_16x16x128_f8f6f4 v[130:133], v[238:245], v[190:197], v[130:133]
	v_mfma_f32_16x16x128_f8f6f4 v[126:129], v[246:253], v[190:197], v[126:129]
	v_mfma_f32_16x16x128_f8f6f4 v[114:117], v[238:245], v[214:221], v[114:117]
	v_mfma_f32_16x16x128_f8f6f4 v[110:113], v[246:253], v[214:221], v[110:113]
	v_mfma_f32_16x16x128_f8f6f4 v[98:101], v[238:245], v[222:229], v[98:101]
	v_mfma_f32_16x16x128_f8f6f4 v[94:97], v[246:253], v[222:229], v[94:97]
	v_mfma_f32_16x16x128_f8f6f4 v[66:69], v[238:245], v[230:237], v[66:69]
	v_mfma_f32_16x16x128_f8f6f4 v[62:65], v[246:253], v[230:237], v[62:65]
	s_setprio 0
	s_mov_b32 m0, s51
	v_lshl_add_u64 v[140:141], v[144:145], 0, s[14:15]
	s_barrier
	ds_read_b128 v[190:193], v159 offset:49152
	ds_read_b128 v[194:197], v159 offset:50176
	ds_read_b128 v[214:217], v159 offset:51200
	ds_read_b128 v[218:221], v159 offset:52224
	ds_read_b128 v[222:225], v159 offset:53248
	ds_read_b128 v[226:229], v159 offset:54272
	ds_read_b128 v[230:233], v159 offset:55296
	ds_read_b128 v[234:237], v159 offset:56320
	global_load_lds_dwordx4 v[140:141], off
	v_lshl_add_u64 v[140:141], v[154:155], 0, s[14:15]
	s_mov_b32 m0, s52
	s_nop 0
	global_load_lds_dwordx4 v[140:141], off
	s_barrier
	s_waitcnt lgkmcnt(0)
	s_setprio 1
	s_waitcnt lgkmcnt(0)
	v_mfma_f32_16x16x128_f8f6f4 v[74:77], v[166:173], v[190:197], v[74:77]
	v_mfma_f32_16x16x128_f8f6f4 v[70:73], v[174:181], v[190:197], v[70:73]
	v_mfma_f32_16x16x128_f8f6f4 v[42:45], v[166:173], v[214:221], v[42:45]
	v_mfma_f32_16x16x128_f8f6f4 v[38:41], v[174:181], v[214:221], v[38:41]
	v_mfma_f32_16x16x128_f8f6f4 v[26:29], v[166:173], v[222:229], v[26:29]
	v_mfma_f32_16x16x128_f8f6f4 v[22:25], v[174:181], v[222:229], v[22:25]
	v_mfma_f32_16x16x128_f8f6f4 v[10:13], v[166:173], v[230:237], v[10:13]
	v_mfma_f32_16x16x128_f8f6f4 v[6:9], v[174:181], v[230:237], v[6:9]
	s_setprio 0
	s_barrier
	s_add_u32 s66, s44, 0x10180
	s_addc_u32 s67, s45, 0
	s_add_i32 s45, s68, s46
	v_lshl_add_u64 v[140:141], s[66:67], 0, v[148:149]
	s_mov_b32 m0, s45
	s_add_i32 s44, s45, 0x2000
	global_load_lds_dwordx4 v[140:141], off
	v_lshl_add_u64 v[140:141], s[66:67], 0, v[152:153]
	s_mov_b32 m0, s44
	s_nop 0
	global_load_lds_dwordx4 v[140:141], off
	s_waitcnt vmcnt(6)
	s_barrier
	s_setprio 1
	v_mfma_f32_16x16x128_f8f6f4 v[82:85], v[238:245], v[190:197], v[82:85]
	v_mfma_f32_16x16x128_f8f6f4 v[78:81], v[246:253], v[190:197], v[78:81]
	v_mfma_f32_16x16x128_f8f6f4 v[50:53], v[238:245], v[214:221], v[50:53]
	v_mfma_f32_16x16x128_f8f6f4 v[46:49], v[246:253], v[214:221], v[46:49]
	v_mfma_f32_16x16x128_f8f6f4 v[34:37], v[238:245], v[222:229], v[34:37]
	v_mfma_f32_16x16x128_f8f6f4 v[30:33], v[246:253], v[222:229], v[30:33]
	v_mfma_f32_16x16x128_f8f6f4 v[18:21], v[238:245], v[230:237], v[18:21]
	v_mfma_f32_16x16x128_f8f6f4 v[14:17], v[246:253], v[230:237], v[14:17]
	s_setprio 0
	s_barrier
	ds_read_b128 v[166:169], v158
	ds_read_b128 v[170:173], v158 offset:1024
	ds_read_b128 v[174:177], v158 offset:2048
	ds_read_b128 v[178:181], v158 offset:3072
	s_add_u32 s42, s42, 0x10180
	s_addc_u32 s43, s43, 0
	s_mov_b32 m0, s65
	v_lshl_add_u64 v[140:141], s[42:43], 0, v[146:147]
	ds_read_b128 v[190:193], v159
	ds_read_b128 v[194:197], v159 offset:1024
	ds_read_b128 v[214:217], v159 offset:2048
	ds_read_b128 v[218:221], v159 offset:3072
	ds_read_b128 v[222:225], v159 offset:4096
	ds_read_b128 v[226:229], v159 offset:5120
	ds_read_b128 v[230:233], v159 offset:6144
	ds_read_b128 v[234:237], v159 offset:7168
	global_load_lds_dwordx4 v[140:141], off
	v_lshl_add_u64 v[140:141], s[42:43], 0, v[150:151]
	s_mov_b32 m0, s29
	s_nop 0
	global_load_lds_dwordx4 v[140:141], off
	s_waitcnt lgkmcnt(8)
	s_barrier
	s_waitcnt lgkmcnt(0)
	s_setprio 1
	s_waitcnt lgkmcnt(0)
	v_mfma_f32_16x16x128_f8f6f4 v[122:125], v[166:173], v[190:197], v[122:125]
	v_mfma_f32_16x16x128_f8f6f4 v[118:121], v[174:181], v[190:197], v[118:121]
	v_mfma_f32_16x16x128_f8f6f4 v[106:109], v[166:173], v[214:221], v[106:109]
	v_mfma_f32_16x16x128_f8f6f4 v[102:105], v[174:181], v[214:221], v[102:105]
	v_mfma_f32_16x16x128_f8f6f4 v[90:93], v[166:173], v[222:229], v[90:93]
	v_mfma_f32_16x16x128_f8f6f4 v[86:89], v[174:181], v[222:229], v[86:89]
	v_mfma_f32_16x16x128_f8f6f4 v[58:61], v[166:173], v[230:237], v[58:61]
	v_mfma_f32_16x16x128_f8f6f4 v[54:57], v[174:181], v[230:237], v[54:57]
	s_setprio 0
	s_barrier
	s_mov_b32 m0, s63
	v_lshl_add_u64 v[140:141], s[4:5], 0, v[148:149]
	ds_read_b128 v[238:241], v161
	ds_read_b128 v[242:245], v161 offset:1024
	ds_read_b128 v[246:249], v161 offset:2048
	ds_read_b128 v[250:253], v161 offset:3072
	global_load_lds_dwordx4 v[140:141], off
	v_lshl_add_u64 v[142:143], s[4:5], 0, v[152:153]
	s_mov_b32 m0, s31
	s_nop 0
	global_load_lds_dwordx4 v[142:143], off
	s_barrier
	s_waitcnt lgkmcnt(0)
	s_setprio 1
	s_waitcnt lgkmcnt(0)
	v_mfma_f32_16x16x128_f8f6f4 v[130:133], v[238:245], v[190:197], v[130:133]
	v_mfma_f32_16x16x128_f8f6f4 v[126:129], v[246:253], v[190:197], v[126:129]
	v_mfma_f32_16x16x128_f8f6f4 v[114:117], v[238:245], v[214:221], v[114:117]
	v_mfma_f32_16x16x128_f8f6f4 v[110:113], v[246:253], v[214:221], v[110:113]
	v_mfma_f32_16x16x128_f8f6f4 v[98:101], v[238:245], v[222:229], v[98:101]
	v_mfma_f32_16x16x128_f8f6f4 v[94:97], v[246:253], v[222:229], v[94:97]
	v_mfma_f32_16x16x128_f8f6f4 v[66:69], v[238:245], v[230:237], v[66:69]
	v_mfma_f32_16x16x128_f8f6f4 v[62:65], v[246:253], v[230:237], v[62:65]
	s_setprio 0
	s_mov_b32 m0, s39
	v_lshl_add_u64 v[144:145], s[40:41], 0, v[146:147]
	s_barrier
	ds_read_b128 v[190:193], v159 offset:16384
	ds_read_b128 v[194:197], v159 offset:17408
	ds_read_b128 v[214:217], v159 offset:18432
	ds_read_b128 v[218:221], v159 offset:19456
	ds_read_b128 v[222:225], v159 offset:20480
	ds_read_b128 v[226:229], v159 offset:21504
	ds_read_b128 v[230:233], v159 offset:22528
	ds_read_b128 v[234:237], v159 offset:23552
	global_load_lds_dwordx4 v[144:145], off
	v_lshl_add_u64 v[154:155], s[40:41], 0, v[150:151]
	s_mov_b32 m0, s48
	s_nop 0
	global_load_lds_dwordx4 v[154:155], off
	s_barrier
	s_waitcnt lgkmcnt(0)
	s_setprio 1
	s_waitcnt lgkmcnt(0)
	v_mfma_f32_16x16x128_f8f6f4 v[74:77], v[166:173], v[190:197], v[74:77]
	v_mfma_f32_16x16x128_f8f6f4 v[70:73], v[174:181], v[190:197], v[70:73]
	v_mfma_f32_16x16x128_f8f6f4 v[42:45], v[166:173], v[214:221], v[42:45]
	v_mfma_f32_16x16x128_f8f6f4 v[38:41], v[174:181], v[214:221], v[38:41]
	v_mfma_f32_16x16x128_f8f6f4 v[26:29], v[166:173], v[222:229], v[26:29]
	v_mfma_f32_16x16x128_f8f6f4 v[22:25], v[174:181], v[222:229], v[22:25]
	v_mfma_f32_16x16x128_f8f6f4 v[10:13], v[166:173], v[230:237], v[10:13]
	v_mfma_f32_16x16x128_f8f6f4 v[6:9], v[174:181], v[230:237], v[6:9]
	s_setprio 0
	s_barrier
	s_add_u32 s42, s4, 0x10000
	s_addc_u32 s43, s5, 0
	s_mov_b32 m0, s61
	v_lshl_add_u64 v[166:167], s[42:43], 0, v[148:149]
	global_load_lds_dwordx4 v[166:167], off
	v_lshl_add_u64 v[166:167], s[42:43], 0, v[152:153]
	s_mov_b32 m0, s60
	s_nop 0
	global_load_lds_dwordx4 v[166:167], off
	s_waitcnt vmcnt(6)
	s_barrier
	s_setprio 1
	v_mfma_f32_16x16x128_f8f6f4 v[82:85], v[238:245], v[190:197], v[82:85]
	v_mfma_f32_16x16x128_f8f6f4 v[78:81], v[246:253], v[190:197], v[78:81]
	v_mfma_f32_16x16x128_f8f6f4 v[50:53], v[238:245], v[214:221], v[50:53]
	v_mfma_f32_16x16x128_f8f6f4 v[46:49], v[246:253], v[214:221], v[46:49]
	v_mfma_f32_16x16x128_f8f6f4 v[34:37], v[238:245], v[222:229], v[34:37]
	v_mfma_f32_16x16x128_f8f6f4 v[30:33], v[246:253], v[222:229], v[30:33]
	v_mfma_f32_16x16x128_f8f6f4 v[18:21], v[238:245], v[230:237], v[18:21]
	v_mfma_f32_16x16x128_f8f6f4 v[14:17], v[246:253], v[230:237], v[14:17]
	s_setprio 0
	s_barrier
	ds_read_b128 v[166:169], v163
	ds_read_b128 v[170:173], v163 offset:1024
	ds_read_b128 v[174:177], v163 offset:2048
	ds_read_b128 v[178:181], v163 offset:3072
	s_add_u32 s40, s40, 0x10000
	s_addc_u32 s41, s41, 0
	s_mov_b32 m0, s49
	v_lshl_add_u64 v[182:183], s[40:41], 0, v[146:147]
	ds_read_b128 v[190:193], v159 offset:32768
	ds_read_b128 v[194:197], v159 offset:33792
	ds_read_b128 v[214:217], v159 offset:34816
	ds_read_b128 v[218:221], v159 offset:35840
	ds_read_b128 v[222:225], v159 offset:36864
	ds_read_b128 v[226:229], v159 offset:37888
	ds_read_b128 v[230:233], v159 offset:38912
	ds_read_b128 v[234:237], v159 offset:39936
	global_load_lds_dwordx4 v[182:183], off
	v_lshl_add_u64 v[182:183], s[40:41], 0, v[150:151]
	s_mov_b32 m0, s50
	s_nop 0
	global_load_lds_dwordx4 v[182:183], off
	s_waitcnt lgkmcnt(8)
	s_barrier
	s_waitcnt lgkmcnt(0)
	s_setprio 1
	s_waitcnt lgkmcnt(0)
	v_mfma_f32_16x16x128_f8f6f4 v[122:125], v[166:173], v[190:197], v[122:125]
	v_mfma_f32_16x16x128_f8f6f4 v[118:121], v[174:181], v[190:197], v[118:121]
	v_mfma_f32_16x16x128_f8f6f4 v[106:109], v[166:173], v[214:221], v[106:109]
	v_mfma_f32_16x16x128_f8f6f4 v[102:105], v[174:181], v[214:221], v[102:105]
	v_mfma_f32_16x16x128_f8f6f4 v[90:93], v[166:173], v[222:229], v[90:93]
	v_mfma_f32_16x16x128_f8f6f4 v[86:89], v[174:181], v[222:229], v[86:89]
	v_mfma_f32_16x16x128_f8f6f4 v[58:61], v[166:173], v[230:237], v[58:61]
	v_mfma_f32_16x16x128_f8f6f4 v[54:57], v[174:181], v[230:237], v[54:57]
	s_setprio 0
	s_barrier
	s_mov_b32 m0, s64
	v_lshl_add_u64 v[140:141], v[140:141], 0, s[12:13]
	ds_read_b128 v[238:241], v164
	ds_read_b128 v[242:245], v164 offset:1024
	ds_read_b128 v[246:249], v164 offset:2048
	ds_read_b128 v[250:253], v164 offset:3072
	global_load_lds_dwordx4 v[140:141], off
	v_lshl_add_u64 v[140:141], v[142:143], 0, s[12:13]
	s_mov_b32 m0, s62
	s_nop 0
	global_load_lds_dwordx4 v[140:141], off
	s_barrier
	s_waitcnt lgkmcnt(0)
	s_setprio 1
	s_waitcnt lgkmcnt(0)
	v_mfma_f32_16x16x128_f8f6f4 v[130:133], v[238:245], v[190:197], v[130:133]
	v_mfma_f32_16x16x128_f8f6f4 v[126:129], v[246:253], v[190:197], v[126:129]
	v_mfma_f32_16x16x128_f8f6f4 v[114:117], v[238:245], v[214:221], v[114:117]
	v_mfma_f32_16x16x128_f8f6f4 v[110:113], v[246:253], v[214:221], v[110:113]
	v_mfma_f32_16x16x128_f8f6f4 v[98:101], v[238:245], v[222:229], v[98:101]
	v_mfma_f32_16x16x128_f8f6f4 v[94:97], v[246:253], v[222:229], v[94:97]
	v_mfma_f32_16x16x128_f8f6f4 v[66:69], v[238:245], v[230:237], v[66:69]
	v_mfma_f32_16x16x128_f8f6f4 v[62:65], v[246:253], v[230:237], v[62:65]
	s_setprio 0
	s_mov_b32 m0, s51
	v_lshl_add_u64 v[140:141], v[144:145], 0, s[12:13]
	s_barrier
	ds_read_b128 v[190:193], v159 offset:49152
	ds_read_b128 v[194:197], v159 offset:50176
	ds_read_b128 v[214:217], v159 offset:51200
	ds_read_b128 v[218:221], v159 offset:52224
	ds_read_b128 v[222:225], v159 offset:53248
	ds_read_b128 v[226:229], v159 offset:54272
	ds_read_b128 v[230:233], v159 offset:55296
	ds_read_b128 v[234:237], v159 offset:56320
	global_load_lds_dwordx4 v[140:141], off
	v_lshl_add_u64 v[140:141], v[154:155], 0, s[12:13]
	s_mov_b32 m0, s52
	s_nop 0
	global_load_lds_dwordx4 v[140:141], off
	s_barrier
	s_waitcnt lgkmcnt(0)
	s_setprio 1
	s_waitcnt lgkmcnt(0)
	v_mfma_f32_16x16x128_f8f6f4 v[74:77], v[166:173], v[190:197], v[74:77]
	v_mfma_f32_16x16x128_f8f6f4 v[70:73], v[174:181], v[190:197], v[70:73]
	v_mfma_f32_16x16x128_f8f6f4 v[42:45], v[166:173], v[214:221], v[42:45]
	v_mfma_f32_16x16x128_f8f6f4 v[38:41], v[174:181], v[214:221], v[38:41]
	v_mfma_f32_16x16x128_f8f6f4 v[26:29], v[166:173], v[222:229], v[26:29]
	v_mfma_f32_16x16x128_f8f6f4 v[22:25], v[174:181], v[222:229], v[22:25]
	v_mfma_f32_16x16x128_f8f6f4 v[10:13], v[166:173], v[230:237], v[10:13]
	v_mfma_f32_16x16x128_f8f6f4 v[6:9], v[174:181], v[230:237], v[6:9]
	s_setprio 0
	s_barrier
	s_add_u32 s4, s4, 0x10080
	s_addc_u32 s5, s5, 0
	s_mov_b32 m0, s45
	v_lshl_add_u64 v[140:141], s[4:5], 0, v[148:149]
	global_load_lds_dwordx4 v[140:141], off
	v_lshl_add_u64 v[140:141], s[4:5], 0, v[152:153]
	s_mov_b32 m0, s44
	s_nop 0
	global_load_lds_dwordx4 v[140:141], off
	s_waitcnt vmcnt(6)
	s_barrier
	s_setprio 1
	v_mfma_f32_16x16x128_f8f6f4 v[82:85], v[238:245], v[190:197], v[82:85]
	v_mfma_f32_16x16x128_f8f6f4 v[78:81], v[246:253], v[190:197], v[78:81]
	v_mfma_f32_16x16x128_f8f6f4 v[50:53], v[238:245], v[214:221], v[50:53]
	v_mfma_f32_16x16x128_f8f6f4 v[46:49], v[246:253], v[214:221], v[46:49]
	v_mfma_f32_16x16x128_f8f6f4 v[34:37], v[238:245], v[222:229], v[34:37]
	v_mfma_f32_16x16x128_f8f6f4 v[30:33], v[246:253], v[222:229], v[30:33]
	v_mfma_f32_16x16x128_f8f6f4 v[18:21], v[238:245], v[230:237], v[18:21]
	v_mfma_f32_16x16x128_f8f6f4 v[14:17], v[246:253], v[230:237], v[14:17]
	s_setprio 0
	v_pk_mul_f32 v[122:123], v[122:123], s[16:17] op_sel_hi:[1,0]
	v_pk_mul_f32 v[118:119], v[118:119], s[16:17] op_sel_hi:[1,0]
	v_med3_f32 v142, v122, s57, v162
	v_med3_f32 v123, v123, s57, v162
	v_mov_b32_e32 v122, 0
	v_cvt_pk_fp8_f32 v122, v142, v123
	v_med3_f32 v118, v118, s57, v162
	v_med3_f32 v119, v119, s57, v162
	v_mov_b32_e32 v123, 0
	v_cvt_pk_fp8_f32 v123, v118, v119
	v_lshl_add_u32 v140, s38, 8, v156
	v_pk_mul_f32 v[124:125], v[124:125], s[16:17] op_sel_hi:[1,0]
	v_pk_mul_f32 v[120:121], v[120:121], s[16:17] op_sel_hi:[1,0]
	v_ashrrev_i32_e32 v141, 31, v140
	v_med3_f32 v124, v124, s57, v162
	v_med3_f32 v125, v125, s57, v162
	v_med3_f32 v118, v120, s57, v162
	v_med3_f32 v119, v121, s57, v162
	s_lshl_b32 s4, s59, 7
	v_cvt_pk_fp8_f32 v122, v124, v125 op_sel:[0,0,1]
	v_cvt_pk_fp8_f32 v123, v118, v119 op_sel:[0,0,1]
	v_lshlrev_b64 v[118:119], 10, v[140:141]
	s_ashr_i32 s5, s4, 31
	v_lshl_add_u64 v[120:121], s[10:11], 0, v[118:119]
	v_lshl_add_u64 v[120:121], v[120:121], 0, s[4:5]
	v_lshl_add_u64 v[120:121], v[120:121], 0, v[134:135]
	s_barrier
	global_store_dwordx2 v[120:121], v[122:123], off
	v_pk_mul_f32 v[122:123], v[130:131], s[18:19] op_sel_hi:[1,0]
	v_pk_mul_f32 v[124:125], v[128:129], s[18:19] op_sel_hi:[1,0]
	v_pk_mul_f32 v[126:127], v[126:127], s[18:19] op_sel_hi:[1,0]
	v_med3_f32 v128, v122, s57, v162
	v_med3_f32 v123, v123, s57, v162
	v_mov_b32_e32 v122, 0
	v_cvt_pk_fp8_f32 v122, v128, v123
	v_med3_f32 v126, v126, s57, v162
	v_med3_f32 v127, v127, s57, v162
	v_mov_b32_e32 v123, 0
	v_cvt_pk_fp8_f32 v123, v126, v127
	v_pk_mul_f32 v[120:121], v[132:133], s[18:19] op_sel_hi:[1,0]
	v_pk_mul_f32 v[106:107], v[106:107], s[16:17] op_sel_hi:[1,0]
	v_med3_f32 v120, v120, s57, v162
	v_med3_f32 v121, v121, s57, v162
	v_cvt_pk_fp8_f32 v122, v120, v121 op_sel:[0,0,1]
	v_med3_f32 v120, v124, s57, v162
	v_med3_f32 v121, v125, s57, v162
	v_cvt_pk_fp8_f32 v123, v120, v121 op_sel:[0,0,1]
	v_lshl_add_u64 v[120:121], s[8:9], 0, v[118:119]
	v_lshl_add_u64 v[120:121], v[120:121], 0, s[4:5]
	v_lshl_add_u64 v[120:121], v[120:121], 0, v[134:135]
	global_store_dwordx2 v[120:121], v[122:123], off
	v_pk_mul_f32 v[102:103], v[102:103], s[16:17] op_sel_hi:[1,0]
	v_med3_f32 v122, v106, s57, v162
	v_med3_f32 v107, v107, s57, v162
	v_mov_b32_e32 v106, 0
	v_cvt_pk_fp8_f32 v106, v122, v107
	v_med3_f32 v102, v102, s57, v162
	v_med3_f32 v103, v103, s57, v162
	v_mov_b32_e32 v107, 0
	v_cvt_pk_fp8_f32 v107, v102, v103
	v_or_b32_e32 v120, 16, v140
	v_pk_mul_f32 v[108:109], v[108:109], s[16:17] op_sel_hi:[1,0]
	v_pk_mul_f32 v[104:105], v[104:105], s[16:17] op_sel_hi:[1,0]
	v_ashrrev_i32_e32 v121, 31, v120
	v_med3_f32 v108, v108, s57, v162
	v_med3_f32 v109, v109, s57, v162
	v_med3_f32 v102, v104, s57, v162
	v_med3_f32 v103, v105, s57, v162
	v_cvt_pk_fp8_f32 v106, v108, v109 op_sel:[0,0,1]
	v_cvt_pk_fp8_f32 v107, v102, v103 op_sel:[0,0,1]
	v_lshlrev_b64 v[102:103], 10, v[120:121]
	v_lshl_add_u64 v[104:105], s[10:11], 0, v[102:103]
	v_lshl_add_u64 v[104:105], v[104:105], 0, s[4:5]
	v_lshl_add_u64 v[104:105], v[104:105], 0, v[134:135]
	global_store_dwordx2 v[104:105], v[106:107], off
	v_pk_mul_f32 v[106:107], v[114:115], s[18:19] op_sel_hi:[1,0]
	v_pk_mul_f32 v[108:109], v[112:113], s[18:19] op_sel_hi:[1,0]
	v_pk_mul_f32 v[110:111], v[110:111], s[18:19] op_sel_hi:[1,0]
	v_med3_f32 v112, v106, s57, v162
	v_med3_f32 v107, v107, s57, v162
	v_mov_b32_e32 v106, 0
	v_cvt_pk_fp8_f32 v106, v112, v107
	v_med3_f32 v110, v110, s57, v162
	v_med3_f32 v111, v111, s57, v162
	v_mov_b32_e32 v107, 0
	v_cvt_pk_fp8_f32 v107, v110, v111
	v_pk_mul_f32 v[104:105], v[116:117], s[18:19] op_sel_hi:[1,0]
	v_pk_mul_f32 v[90:91], v[90:91], s[16:17] op_sel_hi:[1,0]
	v_med3_f32 v104, v104, s57, v162
	v_med3_f32 v105, v105, s57, v162
	v_cvt_pk_fp8_f32 v106, v104, v105 op_sel:[0,0,1]
	v_med3_f32 v104, v108, s57, v162
	v_med3_f32 v105, v109, s57, v162
	v_cvt_pk_fp8_f32 v107, v104, v105 op_sel:[0,0,1]
	v_pk_mul_f32 v[86:87], v[86:87], s[16:17] op_sel_hi:[1,0]
	v_med3_f32 v104, v90, s57, v162
	v_med3_f32 v91, v91, s57, v162
	v_mov_b32_e32 v90, 0
	v_lshl_add_u64 v[102:103], s[8:9], 0, v[102:103]
	v_cvt_pk_fp8_f32 v90, v104, v91
	v_med3_f32 v86, v86, s57, v162
	v_med3_f32 v87, v87, s57, v162
	v_mov_b32_e32 v91, 0
	v_lshl_add_u64 v[102:103], v[102:103], 0, s[4:5]
	v_cvt_pk_fp8_f32 v91, v86, v87
	v_lshl_add_u64 v[102:103], v[102:103], 0, v[134:135]
	global_store_dwordx2 v[102:103], v[106:107], off
	v_or_b32_e32 v102, 32, v140
	v_pk_mul_f32 v[92:93], v[92:93], s[16:17] op_sel_hi:[1,0]
	v_pk_mul_f32 v[88:89], v[88:89], s[16:17] op_sel_hi:[1,0]
	v_ashrrev_i32_e32 v103, 31, v102
	v_med3_f32 v92, v92, s57, v162
	v_med3_f32 v93, v93, s57, v162
	v_med3_f32 v86, v88, s57, v162
	v_med3_f32 v87, v89, s57, v162
	v_cvt_pk_fp8_f32 v90, v92, v93 op_sel:[0,0,1]
	v_cvt_pk_fp8_f32 v91, v86, v87 op_sel:[0,0,1]
	v_lshlrev_b64 v[86:87], 10, v[102:103]
	v_lshl_add_u64 v[88:89], s[10:11], 0, v[86:87]
	v_lshl_add_u64 v[88:89], v[88:89], 0, s[4:5]
	v_lshl_add_u64 v[88:89], v[88:89], 0, v[134:135]
	global_store_dwordx2 v[88:89], v[90:91], off
	v_pk_mul_f32 v[90:91], v[98:99], s[18:19] op_sel_hi:[1,0]
	v_pk_mul_f32 v[92:93], v[96:97], s[18:19] op_sel_hi:[1,0]
	v_pk_mul_f32 v[94:95], v[94:95], s[18:19] op_sel_hi:[1,0]
	v_med3_f32 v96, v90, s57, v162
	v_med3_f32 v91, v91, s57, v162
	v_mov_b32_e32 v90, 0
	v_cvt_pk_fp8_f32 v90, v96, v91
	v_med3_f32 v94, v94, s57, v162
	v_med3_f32 v95, v95, s57, v162
	v_mov_b32_e32 v91, 0
	v_cvt_pk_fp8_f32 v91, v94, v95
	v_pk_mul_f32 v[88:89], v[100:101], s[18:19] op_sel_hi:[1,0]
	v_pk_mul_f32 v[58:59], v[58:59], s[16:17] op_sel_hi:[1,0]
	v_med3_f32 v88, v88, s57, v162
	v_med3_f32 v89, v89, s57, v162
	v_cvt_pk_fp8_f32 v90, v88, v89 op_sel:[0,0,1]
	v_med3_f32 v88, v92, s57, v162
	v_med3_f32 v89, v93, s57, v162
	v_cvt_pk_fp8_f32 v91, v88, v89 op_sel:[0,0,1]
	v_pk_mul_f32 v[54:55], v[54:55], s[16:17] op_sel_hi:[1,0]
	v_med3_f32 v88, v58, s57, v162
	v_med3_f32 v59, v59, s57, v162
	v_mov_b32_e32 v58, 0
	v_lshl_add_u64 v[86:87], s[8:9], 0, v[86:87]
	v_cvt_pk_fp8_f32 v58, v88, v59
	v_med3_f32 v54, v54, s57, v162
	v_med3_f32 v55, v55, s57, v162
	v_mov_b32_e32 v59, 0
	v_lshl_add_u64 v[86:87], v[86:87], 0, s[4:5]
	v_cvt_pk_fp8_f32 v59, v54, v55
	v_lshl_add_u64 v[86:87], v[86:87], 0, v[134:135]
	global_store_dwordx2 v[86:87], v[90:91], off
	v_or_b32_e32 v86, 48, v140
	v_pk_mul_f32 v[60:61], v[60:61], s[16:17] op_sel_hi:[1,0]
	v_pk_mul_f32 v[56:57], v[56:57], s[16:17] op_sel_hi:[1,0]
	v_ashrrev_i32_e32 v87, 31, v86
	v_med3_f32 v60, v60, s57, v162
	v_med3_f32 v61, v61, s57, v162
	v_med3_f32 v54, v56, s57, v162
	v_med3_f32 v55, v57, s57, v162
	v_cvt_pk_fp8_f32 v58, v60, v61 op_sel:[0,0,1]
	v_cvt_pk_fp8_f32 v59, v54, v55 op_sel:[0,0,1]
	v_lshlrev_b64 v[54:55], 10, v[86:87]
	v_lshl_add_u64 v[56:57], s[10:11], 0, v[54:55]
	v_lshl_add_u64 v[56:57], v[56:57], 0, s[4:5]
	v_lshl_add_u64 v[56:57], v[56:57], 0, v[134:135]
	global_store_dwordx2 v[56:57], v[58:59], off
	v_pk_mul_f32 v[58:59], v[66:67], s[18:19] op_sel_hi:[1,0]
	v_pk_mul_f32 v[60:61], v[64:65], s[18:19] op_sel_hi:[1,0]
	v_pk_mul_f32 v[62:63], v[62:63], s[18:19] op_sel_hi:[1,0]
	v_med3_f32 v64, v58, s57, v162
	v_med3_f32 v59, v59, s57, v162
	v_mov_b32_e32 v58, 0
	v_cvt_pk_fp8_f32 v58, v64, v59
	v_med3_f32 v62, v62, s57, v162
	v_med3_f32 v63, v63, s57, v162
	v_mov_b32_e32 v59, 0
	v_cvt_pk_fp8_f32 v59, v62, v63
	v_pk_mul_f32 v[56:57], v[68:69], s[18:19] op_sel_hi:[1,0]
	v_lshl_add_u64 v[54:55], s[8:9], 0, v[54:55]
	v_med3_f32 v56, v56, s57, v162
	v_med3_f32 v57, v57, s57, v162
	v_cvt_pk_fp8_f32 v58, v56, v57 op_sel:[0,0,1]
	v_med3_f32 v56, v60, s57, v162
	v_med3_f32 v57, v61, s57, v162
	v_cvt_pk_fp8_f32 v59, v56, v57 op_sel:[0,0,1]
	v_lshl_add_u64 v[54:55], v[54:55], 0, s[4:5]
	v_lshl_add_u64 v[54:55], v[54:55], 0, v[134:135]
	v_pk_mul_f32 v[62:63], v[70:71], s[16:17] op_sel_hi:[1,0]
	global_store_dwordx2 v[54:55], v[58:59], off
	v_pk_mul_f32 v[58:59], v[74:75], s[16:17] op_sel_hi:[1,0]
	v_med3_f32 v62, v62, s57, v162
	v_med3_f32 v64, v58, s57, v162
	v_med3_f32 v59, v59, s57, v162
	v_mov_b32_e32 v58, 0
	v_cvt_pk_fp8_f32 v58, v64, v59
	v_med3_f32 v63, v63, s57, v162
	v_mov_b32_e32 v59, 0
	v_cvt_pk_fp8_f32 v59, v62, v63
	v_pk_mul_f32 v[56:57], v[76:77], s[16:17] op_sel_hi:[1,0]
	v_pk_mul_f32 v[60:61], v[72:73], s[16:17] op_sel_hi:[1,0]
	v_med3_f32 v56, v56, s57, v162
	v_med3_f32 v57, v57, s57, v162
	s_mov_b64 s[40:41], 0x20000
	v_cvt_pk_fp8_f32 v58, v56, v57 op_sel:[0,0,1]
	v_med3_f32 v56, v60, s57, v162
	v_med3_f32 v57, v61, s57, v162
	v_lshl_add_u64 v[54:55], v[118:119], 0, s[40:41]
	v_cvt_pk_fp8_f32 v59, v56, v57 op_sel:[0,0,1]
	v_lshl_add_u64 v[56:57], s[10:11], 0, v[54:55]
	v_lshl_add_u64 v[56:57], v[56:57], 0, s[4:5]
	v_lshl_add_u64 v[56:57], v[56:57], 0, v[134:135]
	global_store_dwordx2 v[56:57], v[58:59], off
	v_pk_mul_f32 v[58:59], v[82:83], s[18:19] op_sel_hi:[1,0]
	v_pk_mul_f32 v[62:63], v[78:79], s[18:19] op_sel_hi:[1,0]
	v_med3_f32 v64, v58, s57, v162
	v_med3_f32 v59, v59, s57, v162
	v_mov_b32_e32 v58, 0
	v_cvt_pk_fp8_f32 v58, v64, v59
	v_med3_f32 v62, v62, s57, v162
	v_med3_f32 v63, v63, s57, v162
	v_mov_b32_e32 v59, 0
	v_cvt_pk_fp8_f32 v59, v62, v63
	v_pk_mul_f32 v[56:57], v[84:85], s[18:19] op_sel_hi:[1,0]
	v_pk_mul_f32 v[60:61], v[80:81], s[18:19] op_sel_hi:[1,0]
	v_med3_f32 v56, v56, s57, v162
	v_med3_f32 v57, v57, s57, v162
	v_cvt_pk_fp8_f32 v58, v56, v57 op_sel:[0,0,1]
	v_med3_f32 v56, v60, s57, v162
	v_med3_f32 v57, v61, s57, v162
	v_pk_mul_f32 v[42:43], v[42:43], s[16:17] op_sel_hi:[1,0]
	v_cvt_pk_fp8_f32 v59, v56, v57 op_sel:[0,0,1]
	v_pk_mul_f32 v[38:39], v[38:39], s[16:17] op_sel_hi:[1,0]
	v_med3_f32 v56, v42, s57, v162
	v_med3_f32 v43, v43, s57, v162
	v_mov_b32_e32 v42, 0
	v_cvt_pk_fp8_f32 v42, v56, v43
	v_med3_f32 v38, v38, s57, v162
	v_med3_f32 v39, v39, s57, v162
	v_mov_b32_e32 v43, 0
	v_cvt_pk_fp8_f32 v43, v38, v39
	v_lshl_add_u64 v[54:55], s[8:9], 0, v[54:55]
	v_lshl_add_u64 v[54:55], v[54:55], 0, s[4:5]
	v_pk_mul_f32 v[44:45], v[44:45], s[16:17] op_sel_hi:[1,0]
	v_pk_mul_f32 v[40:41], v[40:41], s[16:17] op_sel_hi:[1,0]
	v_lshl_add_u64 v[54:55], v[54:55], 0, v[134:135]
	v_med3_f32 v44, v44, s57, v162
	v_med3_f32 v45, v45, s57, v162
	v_med3_f32 v38, v40, s57, v162
	v_med3_f32 v39, v41, s57, v162
	global_store_dwordx2 v[54:55], v[58:59], off
	v_lshl_add_u64 v[54:55], v[118:119], 0, s[20:21]
	v_cvt_pk_fp8_f32 v42, v44, v45 op_sel:[0,0,1]
	v_cvt_pk_fp8_f32 v43, v38, v39 op_sel:[0,0,1]
	v_pk_mul_f32 v[40:41], v[50:51], s[18:19] op_sel_hi:[1,0]
	v_lshl_add_u64 v[38:39], s[10:11], 0, v[54:55]
	v_pk_mul_f32 v[44:45], v[46:47], s[18:19] op_sel_hi:[1,0]
	v_med3_f32 v46, v40, s57, v162
	v_med3_f32 v41, v41, s57, v162
	v_mov_b32_e32 v40, 0
	v_lshl_add_u64 v[38:39], v[38:39], 0, s[4:5]
	v_cvt_pk_fp8_f32 v40, v46, v41
	v_med3_f32 v44, v44, s57, v162
	v_med3_f32 v45, v45, s57, v162
	v_mov_b32_e32 v41, 0
	v_lshl_add_u64 v[38:39], v[38:39], 0, v[134:135]
	v_cvt_pk_fp8_f32 v41, v44, v45
	global_store_dwordx2 v[38:39], v[42:43], off
	v_pk_mul_f32 v[38:39], v[52:53], s[18:19] op_sel_hi:[1,0]
	v_pk_mul_f32 v[42:43], v[48:49], s[18:19] op_sel_hi:[1,0]
	v_med3_f32 v38, v38, s57, v162
	v_med3_f32 v39, v39, s57, v162
	v_cvt_pk_fp8_f32 v40, v38, v39 op_sel:[0,0,1]
	v_med3_f32 v38, v42, s57, v162
	v_med3_f32 v39, v43, s57, v162
	v_cvt_pk_fp8_f32 v41, v38, v39 op_sel:[0,0,1]
	v_lshl_add_u64 v[38:39], s[8:9], 0, v[54:55]
	v_lshl_add_u64 v[38:39], v[38:39], 0, s[4:5]
	v_lshl_add_u64 v[38:39], v[38:39], 0, v[134:135]
	v_pk_mul_f32 v[26:27], v[26:27], s[16:17] op_sel_hi:[1,0]
	global_store_dwordx2 v[38:39], v[40:41], off
	v_pk_mul_f32 v[22:23], v[22:23], s[16:17] op_sel_hi:[1,0]
	v_med3_f32 v40, v26, s57, v162
	v_med3_f32 v27, v27, s57, v162
	v_mov_b32_e32 v26, 0
	v_cvt_pk_fp8_f32 v26, v40, v27
	v_med3_f32 v22, v22, s57, v162
	v_med3_f32 v23, v23, s57, v162
	v_mov_b32_e32 v27, 0
	v_cvt_pk_fp8_f32 v27, v22, v23
	v_pk_mul_f32 v[28:29], v[28:29], s[16:17] op_sel_hi:[1,0]
	v_pk_mul_f32 v[24:25], v[24:25], s[16:17] op_sel_hi:[1,0]
	v_med3_f32 v28, v28, s57, v162
	v_med3_f32 v29, v29, s57, v162
	v_med3_f32 v22, v24, s57, v162
	v_med3_f32 v23, v25, s57, v162
	v_lshl_add_u64 v[38:39], v[118:119], 0, s[22:23]
	v_cvt_pk_fp8_f32 v26, v28, v29 op_sel:[0,0,1]
	v_cvt_pk_fp8_f32 v27, v22, v23 op_sel:[0,0,1]
	v_pk_mul_f32 v[24:25], v[34:35], s[18:19] op_sel_hi:[1,0]
	v_lshl_add_u64 v[22:23], s[10:11], 0, v[38:39]
	v_pk_mul_f32 v[28:29], v[30:31], s[18:19] op_sel_hi:[1,0]
	v_med3_f32 v30, v24, s57, v162
	v_med3_f32 v25, v25, s57, v162
	v_mov_b32_e32 v24, 0
	v_lshl_add_u64 v[22:23], v[22:23], 0, s[4:5]
	v_cvt_pk_fp8_f32 v24, v30, v25
	v_med3_f32 v28, v28, s57, v162
	v_med3_f32 v29, v29, s57, v162
	v_mov_b32_e32 v25, 0
	v_lshl_add_u64 v[22:23], v[22:23], 0, v[134:135]
	v_cvt_pk_fp8_f32 v25, v28, v29
	global_store_dwordx2 v[22:23], v[26:27], off
	v_pk_mul_f32 v[22:23], v[36:37], s[18:19] op_sel_hi:[1,0]
	v_pk_mul_f32 v[26:27], v[32:33], s[18:19] op_sel_hi:[1,0]
	v_med3_f32 v22, v22, s57, v162
	v_med3_f32 v23, v23, s57, v162
	v_cvt_pk_fp8_f32 v24, v22, v23 op_sel:[0,0,1]
	v_med3_f32 v22, v26, s57, v162
	v_med3_f32 v23, v27, s57, v162
	v_cvt_pk_fp8_f32 v25, v22, v23 op_sel:[0,0,1]
	v_lshl_add_u64 v[22:23], s[8:9], 0, v[38:39]
	v_lshl_add_u64 v[22:23], v[22:23], 0, s[4:5]
	v_lshl_add_u64 v[22:23], v[22:23], 0, v[134:135]
	v_pk_mul_f32 v[10:11], v[10:11], s[16:17] op_sel_hi:[1,0]
	global_store_dwordx2 v[22:23], v[24:25], off
	v_pk_mul_f32 v[6:7], v[6:7], s[16:17] op_sel_hi:[1,0]
	v_med3_f32 v24, v10, s57, v162
	v_med3_f32 v11, v11, s57, v162
	v_mov_b32_e32 v10, 0
	v_cvt_pk_fp8_f32 v10, v24, v11
	v_med3_f32 v6, v6, s57, v162
	v_med3_f32 v7, v7, s57, v162
	v_mov_b32_e32 v11, 0
	v_cvt_pk_fp8_f32 v11, v6, v7
	v_pk_mul_f32 v[12:13], v[12:13], s[16:17] op_sel_hi:[1,0]
	v_pk_mul_f32 v[8:9], v[8:9], s[16:17] op_sel_hi:[1,0]
	v_med3_f32 v12, v12, s57, v162
	v_med3_f32 v13, v13, s57, v162
	v_med3_f32 v6, v8, s57, v162
	v_med3_f32 v7, v9, s57, v162
	v_lshl_add_u64 v[22:23], v[118:119], 0, s[24:25]
	v_cvt_pk_fp8_f32 v10, v12, v13 op_sel:[0,0,1]
	v_cvt_pk_fp8_f32 v11, v6, v7 op_sel:[0,0,1]
	v_pk_mul_f32 v[8:9], v[18:19], s[18:19] op_sel_hi:[1,0]
	v_lshl_add_u64 v[6:7], s[10:11], 0, v[22:23]
	v_pk_mul_f32 v[12:13], v[14:15], s[18:19] op_sel_hi:[1,0]
	v_med3_f32 v14, v8, s57, v162
	v_med3_f32 v9, v9, s57, v162
	v_mov_b32_e32 v8, 0
	v_lshl_add_u64 v[6:7], v[6:7], 0, s[4:5]
	v_cvt_pk_fp8_f32 v8, v14, v9
	v_med3_f32 v12, v12, s57, v162
	v_med3_f32 v13, v13, s57, v162
	v_mov_b32_e32 v9, 0
	v_lshl_add_u64 v[6:7], v[6:7], 0, v[134:135]
	v_cvt_pk_fp8_f32 v9, v12, v13
	global_store_dwordx2 v[6:7], v[10:11], off
	v_pk_mul_f32 v[6:7], v[20:21], s[18:19] op_sel_hi:[1,0]
	v_pk_mul_f32 v[10:11], v[16:17], s[18:19] op_sel_hi:[1,0]
	v_med3_f32 v6, v6, s57, v162
	v_med3_f32 v7, v7, s57, v162
	v_cvt_pk_fp8_f32 v8, v6, v7 op_sel:[0,0,1]
	v_med3_f32 v6, v10, s57, v162
	v_med3_f32 v7, v11, s57, v162
	v_cvt_pk_fp8_f32 v9, v6, v7 op_sel:[0,0,1]
	v_lshl_add_u64 v[6:7], s[8:9], 0, v[22:23]
	v_lshl_add_u64 v[6:7], v[6:7], 0, s[4:5]
	v_readlane_b32 s40, v254, 42
	v_lshl_add_u64 v[6:7], v[6:7], 0, v[134:135]
	s_add_i32 s54, s54, s40
	s_andn2_b64 vcc, exec, s[0:1]
	s_mov_b32 s59, s28
	s_mov_b32 s38, s30
	s_mov_b64 s[44:45], s[36:37]
	s_mov_b64 s[42:43], s[34:35]
	global_store_dwordx2 v[6:7], v[8:9], off
	v_readlane_b32 s41, v254, 43
	s_cbranch_vccz .LBB0_954

.LBB0_1230:
	ds_read_b128 v[2:5], v190
	ds_read_b128 v[6:9], v190 offset:1024
	ds_read_b128 v[10:13], v190 offset:2048
	ds_read_b128 v[14:17], v190 offset:3072
	s_add_u32 s26, s24, 0xfffc0080
	s_addc_u32 s27, s25, -1
	s_cmp_eq_u32 s48, 12
	s_cselect_b32 s29, s6, s27
	s_cselect_b32 s28, s17, s26
	s_cselect_b32 s27, s15, s31
	s_cselect_b32 s26, s23, s30
	s_add_i32 m0, s35, 0xc000
	ds_read_b128 v[194:197], v191
	ds_read_b128 v[198:201], v191 offset:1024
	ds_read_b128 v[214:217], v191 offset:2048
	ds_read_b128 v[218:221], v191 offset:3072
	ds_read_b128 v[222:225], v191 offset:4096
	ds_read_b128 v[226:229], v191 offset:5120
	ds_read_b128 v[230:233], v191 offset:6144
	ds_read_b128 v[234:237], v191 offset:7168
	global_load_lds_dwordx4 v170, s[24:25]
	s_add_i32 m0, s35, 0xe000
	s_nop 0
	global_load_lds_dwordx4 v172, s[24:25]
	s_waitcnt lgkmcnt(8)
	s_barrier
	s_waitcnt lgkmcnt(0)
	s_setprio 1
	s_waitcnt lgkmcnt(0)
	v_mfma_f32_16x16x128_f8f6f4 v[142:145], v[2:9], v[194:201], v[142:145]
	v_mfma_f32_16x16x128_f8f6f4 v[138:141], v[10:17], v[194:201], v[138:141]
	v_mfma_f32_16x16x128_f8f6f4 v[126:129], v[2:9], v[214:221], v[126:129]
	v_mfma_f32_16x16x128_f8f6f4 v[122:125], v[10:17], v[214:221], v[122:125]
	v_mfma_f32_16x16x128_f8f6f4 v[110:113], v[2:9], v[222:229], v[110:113]
	v_mfma_f32_16x16x128_f8f6f4 v[106:109], v[10:17], v[222:229], v[106:109]
	v_mfma_f32_16x16x128_f8f6f4 v[94:97], v[2:9], v[230:237], v[94:97]
	v_mfma_f32_16x16x128_f8f6f4 v[90:93], v[10:17], v[230:237], v[90:93]
	s_setprio 0
	s_barrier
	s_add_i32 s49, s44, s34
	s_add_u32 s66, s26, 0x80
	s_addc_u32 s67, s27, 0
	s_mov_b32 m0, s49
	ds_read_b128 v[238:241], v193
	ds_read_b128 v[242:245], v193 offset:1024
	ds_read_b128 v[246:249], v193 offset:2048
	ds_read_b128 v[250:253], v193 offset:3072
	global_load_lds_dwordx4 v148, s[26:27]
	s_add_i32 m0, s49, 0x2000
	s_nop 0
	global_load_lds_dwordx4 v152, s[26:27]
	s_barrier
	s_waitcnt lgkmcnt(0)
	s_setprio 1
	s_waitcnt lgkmcnt(0)
	v_mfma_f32_16x16x128_f8f6f4 v[134:137], v[238:245], v[194:201], v[134:137]
	v_mfma_f32_16x16x128_f8f6f4 v[130:133], v[246:253], v[194:201], v[130:133]
	v_mfma_f32_16x16x128_f8f6f4 v[118:121], v[238:245], v[214:221], v[118:121]
	v_mfma_f32_16x16x128_f8f6f4 v[114:117], v[246:253], v[214:221], v[114:117]
	v_mfma_f32_16x16x128_f8f6f4 v[102:105], v[238:245], v[222:229], v[102:105]
	v_mfma_f32_16x16x128_f8f6f4 v[98:101], v[246:253], v[222:229], v[98:101]
	v_mfma_f32_16x16x128_f8f6f4 v[86:89], v[238:245], v[230:237], v[86:89]
	v_mfma_f32_16x16x128_f8f6f4 v[82:85], v[246:253], v[230:237], v[82:85]
	s_setprio 0
	s_mov_b32 m0, s35
	s_add_u32 s68, s28, 0x80
	s_addc_u32 s69, s29, 0
	s_barrier
	ds_read_b128 v[194:197], v191 offset:16384
	ds_read_b128 v[198:201], v191 offset:17408
	ds_read_b128 v[214:217], v191 offset:18432
	ds_read_b128 v[218:221], v191 offset:19456
	ds_read_b128 v[222:225], v191 offset:20480
	ds_read_b128 v[226:229], v191 offset:21504
	ds_read_b128 v[230:233], v191 offset:22528
	ds_read_b128 v[234:237], v191 offset:23552
	global_load_lds_dwordx4 v146, s[28:29]
	s_mov_b32 m0, s36
	s_nop 0
	global_load_lds_dwordx4 v150, s[28:29]
	s_barrier
	s_waitcnt lgkmcnt(0)
	s_setprio 1
	s_waitcnt lgkmcnt(0)
	v_mfma_f32_16x16x128_f8f6f4 v[78:81], v[2:9], v[194:201], v[78:81]
	v_mfma_f32_16x16x128_f8f6f4 v[74:77], v[10:17], v[194:201], v[74:77]
	v_mfma_f32_16x16x128_f8f6f4 v[62:65], v[2:9], v[214:221], v[62:65]
	v_mfma_f32_16x16x128_f8f6f4 v[58:61], v[10:17], v[214:221], v[58:61]
	v_mfma_f32_16x16x128_f8f6f4 v[46:49], v[2:9], v[222:229], v[46:49]
	v_mfma_f32_16x16x128_f8f6f4 v[42:45], v[10:17], v[222:229], v[42:45]
	v_mfma_f32_16x16x128_f8f6f4 v[30:33], v[2:9], v[230:237], v[30:33]
	v_mfma_f32_16x16x128_f8f6f4 v[26:29], v[10:17], v[230:237], v[26:29]
	s_setprio 0
	s_barrier
	s_add_u32 s50, s26, 0x40000
	s_addc_u32 s51, s27, 0
	s_add_i32 s49, s45, s34
	s_mov_b32 m0, s49
	s_nop 0
	global_load_lds_dwordx4 v148, s[50:51]
	s_add_i32 m0, s49, 0x2000
	s_nop 0
	global_load_lds_dwordx4 v152, s[50:51]
	s_waitcnt vmcnt(6)
	s_barrier
	s_setprio 1
	v_mfma_f32_16x16x128_f8f6f4 v[70:73], v[238:245], v[194:201], v[70:73]
	v_mfma_f32_16x16x128_f8f6f4 v[66:69], v[246:253], v[194:201], v[66:69]
	v_mfma_f32_16x16x128_f8f6f4 v[54:57], v[238:245], v[214:221], v[54:57]
	v_mfma_f32_16x16x128_f8f6f4 v[50:53], v[246:253], v[214:221], v[50:53]
	v_mfma_f32_16x16x128_f8f6f4 v[38:41], v[238:245], v[222:229], v[38:41]
	v_mfma_f32_16x16x128_f8f6f4 v[34:37], v[246:253], v[222:229], v[34:37]
	v_mfma_f32_16x16x128_f8f6f4 v[22:25], v[238:245], v[230:237], v[22:25]
	v_mfma_f32_16x16x128_f8f6f4 v[18:21], v[246:253], v[230:237], v[18:21]
	s_setprio 0
	s_add_i32 s49, 0, 0x18000
	v_add_u32_e32 v14, s49, v186
	s_barrier
	ds_read_b128 v[2:5], v14
	ds_read_b128 v[6:9], v14 offset:1024
	ds_read_b128 v[10:13], v14 offset:2048
	ds_read_b128 v[14:17], v14 offset:3072
	s_add_u32 s28, s28, 0x40000
	s_addc_u32 s29, s29, 0
	s_mov_b32 m0, s37
	ds_read_b128 v[194:197], v191 offset:32768
	ds_read_b128 v[198:201], v191 offset:33792
	ds_read_b128 v[214:217], v191 offset:34816
	ds_read_b128 v[218:221], v191 offset:35840
	ds_read_b128 v[222:225], v191 offset:36864
	ds_read_b128 v[226:229], v191 offset:37888
	ds_read_b128 v[230:233], v191 offset:38912
	ds_read_b128 v[234:237], v191 offset:39936
	global_load_lds_dwordx4 v146, s[28:29]
	s_mov_b32 m0, s38
	s_nop 0
	global_load_lds_dwordx4 v150, s[28:29]
	s_waitcnt lgkmcnt(8)
	s_barrier
	s_waitcnt lgkmcnt(0)
	s_setprio 1
	s_waitcnt lgkmcnt(0)
	v_mfma_f32_16x16x128_f8f6f4 v[142:145], v[2:9], v[194:201], v[142:145]
	v_mfma_f32_16x16x128_f8f6f4 v[138:141], v[10:17], v[194:201], v[138:141]
	v_mfma_f32_16x16x128_f8f6f4 v[126:129], v[2:9], v[214:221], v[126:129]
	v_mfma_f32_16x16x128_f8f6f4 v[122:125], v[10:17], v[214:221], v[122:125]
	v_mfma_f32_16x16x128_f8f6f4 v[110:113], v[2:9], v[222:229], v[110:113]
	v_mfma_f32_16x16x128_f8f6f4 v[106:109], v[10:17], v[222:229], v[106:109]
	v_mfma_f32_16x16x128_f8f6f4 v[94:97], v[2:9], v[230:237], v[94:97]
	v_mfma_f32_16x16x128_f8f6f4 v[90:93], v[10:17], v[230:237], v[90:93]
	s_setprio 0
	s_barrier
	s_add_i32 s28, 0, 0x1c000
	s_add_i32 s29, s49, s34
	v_add_u32_e32 v202, s28, v186
	s_mov_b32 m0, s29
	ds_read_b128 v[238:241], v202
	ds_read_b128 v[242:245], v202 offset:1024
	ds_read_b128 v[246:249], v202 offset:2048
	ds_read_b128 v[250:253], v202 offset:3072
	global_load_lds_dwordx4 v148, s[66:67]
	s_add_i32 m0, s29, 0x2000
	s_nop 0
	global_load_lds_dwordx4 v152, s[66:67]
	s_barrier
	s_waitcnt lgkmcnt(0)
	s_setprio 1
	s_waitcnt lgkmcnt(0)
	v_mfma_f32_16x16x128_f8f6f4 v[134:137], v[238:245], v[194:201], v[134:137]
	v_mfma_f32_16x16x128_f8f6f4 v[130:133], v[246:253], v[194:201], v[130:133]
	v_mfma_f32_16x16x128_f8f6f4 v[118:121], v[238:245], v[214:221], v[118:121]
	v_mfma_f32_16x16x128_f8f6f4 v[114:117], v[246:253], v[214:221], v[114:117]
	v_mfma_f32_16x16x128_f8f6f4 v[102:105], v[238:245], v[222:229], v[102:105]
	v_mfma_f32_16x16x128_f8f6f4 v[98:101], v[246:253], v[222:229], v[98:101]
	v_mfma_f32_16x16x128_f8f6f4 v[86:89], v[238:245], v[230:237], v[86:89]
	v_mfma_f32_16x16x128_f8f6f4 v[82:85], v[246:253], v[230:237], v[82:85]
	s_setprio 0
	s_mov_b32 m0, s41
	s_barrier
	ds_read_b128 v[194:197], v191 offset:49152
	ds_read_b128 v[198:201], v191 offset:50176
	ds_read_b128 v[214:217], v191 offset:51200
	ds_read_b128 v[218:221], v191 offset:52224
	ds_read_b128 v[222:225], v191 offset:53248
	ds_read_b128 v[226:229], v191 offset:54272
	ds_read_b128 v[230:233], v191 offset:55296
	ds_read_b128 v[234:237], v191 offset:56320
	global_load_lds_dwordx4 v146, s[68:69]
	s_mov_b32 m0, s42
	s_nop 0
	global_load_lds_dwordx4 v150, s[68:69]
	s_barrier
	s_waitcnt lgkmcnt(0)
	s_setprio 1
	s_waitcnt lgkmcnt(0)
	v_mfma_f32_16x16x128_f8f6f4 v[78:81], v[2:9], v[194:201], v[78:81]
	v_mfma_f32_16x16x128_f8f6f4 v[74:77], v[10:17], v[194:201], v[74:77]
	v_mfma_f32_16x16x128_f8f6f4 v[62:65], v[2:9], v[214:221], v[62:65]
	v_mfma_f32_16x16x128_f8f6f4 v[58:61], v[10:17], v[214:221], v[58:61]
	v_mfma_f32_16x16x128_f8f6f4 v[46:49], v[2:9], v[222:229], v[46:49]
	v_mfma_f32_16x16x128_f8f6f4 v[42:45], v[10:17], v[222:229], v[42:45]
	v_mfma_f32_16x16x128_f8f6f4 v[30:33], v[2:9], v[230:237], v[30:33]
	v_mfma_f32_16x16x128_f8f6f4 v[26:29], v[10:17], v[230:237], v[26:29]
	s_setprio 0
	s_barrier
	s_add_u32 s26, s26, 0x40080
	s_addc_u32 s27, s27, 0
	s_add_i32 s28, s28, s34
	s_mov_b32 m0, s28
	s_nop 0
	global_load_lds_dwordx4 v148, s[26:27]
	s_add_i32 m0, s28, 0x2000
	s_nop 0
	global_load_lds_dwordx4 v152, s[26:27]
	s_waitcnt vmcnt(6)
	s_barrier
	s_setprio 1
	v_mfma_f32_16x16x128_f8f6f4 v[70:73], v[238:245], v[194:201], v[70:73]
	v_mfma_f32_16x16x128_f8f6f4 v[66:69], v[246:253], v[194:201], v[66:69]
	v_mfma_f32_16x16x128_f8f6f4 v[54:57], v[238:245], v[214:221], v[54:57]
	v_mfma_f32_16x16x128_f8f6f4 v[50:53], v[246:253], v[214:221], v[50:53]
	v_mfma_f32_16x16x128_f8f6f4 v[38:41], v[238:245], v[222:229], v[38:41]
	v_mfma_f32_16x16x128_f8f6f4 v[34:37], v[246:253], v[222:229], v[34:37]
	v_mfma_f32_16x16x128_f8f6f4 v[22:25], v[238:245], v[230:237], v[22:25]
	v_mfma_f32_16x16x128_f8f6f4 v[18:21], v[246:253], v[230:237], v[18:21]
	s_setprio 0
	s_add_i32 s48, s48, 2
	s_add_u32 s24, s24, 0x100
	s_addc_u32 s25, s25, 0
	s_add_u32 s30, s30, 0x100
	s_addc_u32 s31, s31, 0
	s_cmp_gt_u32 s48, 13
	s_barrier
	s_cbranch_scc0 .LBB0_1230
	s_lshl_b32 s26, s22, 8
	s_cmpk_gt_i32 s22, 0x7f
	s_mov_b64 s[30:31], -1
	s_cbranch_scc0 .LBB0_1233
	s_add_i32 s6, s26, 0xffff8000
	s_mov_b32 s27, s7
	s_lshl_b64 s[28:29], s[6:7], 12
	s_lshl_b64 s[24:25], s[26:27], 12
	s_mov_b64 s[30:31], 0
